# v55 + P2a gate weights lw[row] for the four epilogue m-tile blocks prefetched in the pass prologue (epilogue blocks no longer load and wait)
# baseline (speedup 1.0000x reference)
.LBB0_263:
	s_sub_i32 s7, s62, s64
	v_mov_b32_e32 v162, v0
	s_min_i32 s7, s7, 0x200
	s_add_i32 s8, s7, 0x7f
	v_readfirstlane_b32 s6, v162
	s_lshr_b32 s66, s8, 7
	s_ashr_i32 s8, s6, 2
	s_and_b32 s8, s8, -16
	s_mul_i32 s8, s8, s66
	s_add_i32 s8, s8, s64
	v_bfe_u32 v2, v162, 3, 3
	v_or_b32_e32 v10, s8, v2
	s_add_i32 s65, s7, s64
	v_mov_b32_e32 v11, s64
	v_cmp_gt_i32_e32 vcc, s65, v10
	v_or_b32_e32 v4, 8, v10
	v_add_u32_e32 v6, 16, v10
	v_cndmask_b32_e32 v2, v11, v10, vcc
	v_cmp_gt_i32_e32 vcc, s65, v4
	s_cmpk_gt_u32 s7, 0x80
	s_cselect_b64 s[46:47], -1, 0
	v_cndmask_b32_e32 v4, v11, v4, vcc
	v_cmp_gt_i32_e32 vcc, s65, v6
	s_and_b64 vcc, s[46:47], vcc
	v_add_u32_e32 v8, 24, v10
	v_cndmask_b32_e32 v6, v11, v6, vcc
	v_cmp_gt_i32_e32 vcc, s65, v8
	s_and_b64 vcc, s[46:47], vcc
	v_ashrrev_i32_e32 v3, 31, v2
	v_ashrrev_i32_e32 v7, 31, v6
	v_cndmask_b32_e32 v8, v11, v8, vcc
	v_lshl_add_u64 v[2:3], v[2:3], 2, s[24:25]
	v_ashrrev_i32_e32 v5, 31, v4
	v_lshl_add_u64 v[6:7], v[6:7], 2, s[24:25]
	v_ashrrev_i32_e32 v9, 31, v8
	v_lshl_add_u64 v[4:5], v[4:5], 2, s[24:25]
	v_lshl_add_u64 v[8:9], v[8:9], 2, s[24:25]
	global_load_dword v12, v[2:3], off
	global_load_dword v13, v[4:5], off
	s_nop 0
	global_load_dword v6, v[6:7], off
	s_nop 0
	global_load_dword v7, v[8:9], off
	v_add_u32_e32 v2, 32, v10
	s_cmpk_gt_u32 s7, 0x100
	s_cselect_b64 s[44:45], -1, 0
	v_cmp_gt_i32_e32 vcc, s65, v2
	s_and_b64 vcc, s[44:45], vcc
	v_add_u32_e32 v4, 40, v10
	v_cndmask_b32_e32 v2, v11, v2, vcc
	v_cmp_gt_i32_e32 vcc, s65, v4
	s_and_b64 vcc, s[44:45], vcc
	v_ashrrev_i32_e32 v3, 31, v2
	v_cndmask_b32_e32 v4, v11, v4, vcc
	v_lshl_add_u64 v[2:3], v[2:3], 2, s[24:25]
	v_ashrrev_i32_e32 v5, 31, v4
	v_lshl_add_u64 v[4:5], v[4:5], 2, s[24:25]
	global_load_dword v8, v[2:3], off
	global_load_dword v9, v[4:5], off
	v_add_u32_e32 v2, 48, v10
	s_cmpk_gt_u32 s7, 0x180
	s_cselect_b64 s[42:43], -1, 0
	v_cmp_gt_i32_e32 vcc, s65, v2
	s_and_b64 vcc, s[42:43], vcc
	v_add_u32_e32 v4, 56, v10
	v_cndmask_b32_e32 v2, v11, v2, vcc
	v_cmp_gt_i32_e32 vcc, s65, v4
	s_and_b64 vcc, s[42:43], vcc
	v_ashrrev_i32_e32 v3, 31, v2
	v_cndmask_b32_e32 v4, v11, v4, vcc
	v_lshl_add_u64 v[2:3], v[2:3], 2, s[24:25]
	v_ashrrev_i32_e32 v5, 31, v4
	v_lshl_add_u64 v[4:5], v[4:5], 2, s[24:25]
	global_load_dword v131, v[2:3], off
	global_load_dword v130, v[4:5], off
	v_and_b32_e32 v10, 31, v162
	v_and_b32_e32 v2, 7, v162
	v_bfe_u32 v3, v162, 4, 2
	v_cmp_gt_u32_e32 vcc, 16, v10
	v_bitop3_b32 v2, v3, v2, 4 bitop3:0x36
	v_ashrrev_i32_e32 v11, 5, v162
	v_cndmask_b32_e32 v15, v166, v167, vcc
	v_bitop3_b32 v14, v3, v162, 7 bitop3:0x78
	v_lshlrev_b32_e32 v132, 4, v2
	v_lshl_add_u32 v2, v10, 4, v15
	v_lshlrev_b32_e32 v133, 4, v14
	v_lshl_or_b32 v168, v11, 13, v2
	global_load_dwordx4 v[228:231], v168, s[22:23]
	global_load_dwordx4 v[232:235], v168, s[22:23] offset:2048
	global_load_dwordx4 v[236:239], v168, s[28:29]
	global_load_dwordx4 v[240:243], v168, s[28:29] offset:2048
	global_load_dwordx4 v[60:63], v168, s[30:31]
	global_load_dwordx4 v[64:67], v168, s[30:31] offset:2048
	global_load_dwordx4 v[68:71], v168, s[34:35]
	global_load_dwordx4 v[72:75], v168, s[34:35] offset:2048
	v_readfirstlane_b32 vcc_lo, v162
	s_ashr_i32 vcc_lo, vcc_lo, 6
	s_mul_i32 vcc_lo, s66, vcc_lo
	s_lshl_b32 vcc_lo, vcc_lo, 4
	v_and_or_b32 v252, v162, 15, s64
	v_add_u32_e32 v252, vcc_lo, v252
	v_lshlrev_b32_e32 v252, 2, v252
	global_load_dword v244, v252, s[26:27]
	global_load_dword v245, v252, s[26:27] offset:64
	global_load_dword v246, v252, s[26:27] offset:128
	global_load_dword v247, v252, s[26:27] offset:192
	v_lshrrev_b32_e32 v5, 4, v162
	v_lshlrev_b32_e32 v3, 11, v3
	s_lshl_b32 s6, s6, 8
	s_and_b32 s6, s6, 0xffffc000
	v_and_b32_e32 v4, 15, v162
	s_add_i32 s67, s6, 0
	s_add_i32 s68, s67, 0x400
	s_mov_b64 s[6:7], -1
	s_mov_b64 s[8:9], 0
	s_cmp_lt_i32 s66, 2
	s_mov_b64 s[10:11], 0
	s_waitcnt vmcnt(19)
	v_lshlrev_b32_e32 v2, 8, v12
	v_and_or_b32 v169, v2, s60, v133
	s_waitcnt vmcnt(18)
	v_lshlrev_b32_e32 v2, 8, v13
	v_and_or_b32 v170, v2, s60, v132
	s_waitcnt vmcnt(17)
	v_lshlrev_b32_e32 v2, 8, v6
	s_waitcnt vmcnt(16)
	v_lshlrev_b32_e32 v6, 8, v7
	v_and_or_b32 v175, v6, s60, v132
	v_and_or_b32 v174, v2, s60, v133
	s_waitcnt vmcnt(15)
	v_lshlrev_b32_e32 v2, 8, v8
	s_waitcnt vmcnt(14)
	v_lshlrev_b32_e32 v6, 8, v9
	v_and_or_b32 v177, v6, s60, v132
	v_lshlrev_b32_e32 v6, 3, v162
	v_and_or_b32 v176, v2, s60, v133
	v_lshlrev_b32_e32 v2, 10, v11
	v_and_b32_e32 v6, 24, v6
	v_add3_u32 v173, s61, v2, v6
	v_bfe_u32 v2, v162, 2, 3
	v_bitop3_b32 v134, v2, v5, 4 bitop3:0x78
	v_bfe_u32 v2, v162, 2, 2
	v_lshlrev_b32_e32 v7, 8, v2
	v_add3_u32 v3, s61, v3, v7
	v_lshrrev_b32_e32 v7, 2, v162
	v_and_or_b32 v2, v7, 4, v2
	v_lshlrev_b32_e32 v2, 5, v2
	v_add3_u32 v171, v3, v6, v2
	v_bfe_u32 v3, v162, 1, 3
	v_bitop3_b32 v3, v5, v3, 3 bitop3:0x6c
	v_lshlrev_b32_e32 v2, 7, v4
	v_lshlrev_b32_e32 v3, 4, v3
	v_add3_u32 v172, s67, v2, v3
	s_cbranch_scc1 .LBB0_275
	s_cmp_gt_i32 s66, 2
	s_cbranch_scc0 .LBB0_269
	s_cmp_eq_u32 s66, 3
	s_mov_b64 s[10:11], -1
	s_cbranch_scc0 .LBB0_270
	s_mov_b32 s6, m0
	s_mov_b32 m0, s67
	s_nop 0
	global_load_lds_dwordx4 v169, s[18:19]
	s_mov_b32 m0, s6
	s_add_i32 s52, s67, 0x800
	s_mov_b32 s6, m0
	s_mov_b32 m0, s68
	s_nop 0
	global_load_lds_dwordx4 v170, s[18:19]
	s_mov_b32 m0, s6
	s_add_i32 s53, s67, 0xc00
	s_mov_b32 s6, m0
	s_mov_b32 m0, s52
	s_nop 0
	global_load_lds_dwordx4 v174, s[18:19]
	s_mov_b32 m0, s6
	s_add_i32 s69, s67, 0x1000
	s_mov_b32 s6, m0
	s_mov_b32 m0, s53
	s_nop 0
	global_load_lds_dwordx4 v175, s[18:19]
	s_mov_b32 m0, s6
	s_add_i32 s70, s67, 0x1400
	s_mov_b32 s6, m0
	s_mov_b32 m0, s69
	s_nop 0
	global_load_lds_dwordx4 v176, s[18:19]
	s_mov_b32 m0, s6
	v_mov_b32_e32 v26, 0
	s_mov_b32 s6, m0
	s_mov_b32 m0, s70
	s_nop 0
	global_load_lds_dwordx4 v177, s[18:19]
	s_mov_b32 m0, s6
	s_waitcnt vmcnt(10)
	v_mov_b32_e32 v106, v60
	v_mov_b32_e32 v107, v61
	v_mov_b32_e32 v108, v62
	v_mov_b32_e32 v109, v63
	v_mov_b32_e32 v102, v64
	v_mov_b32_e32 v103, v65
	v_mov_b32_e32 v104, v66
	v_mov_b32_e32 v105, v67
	v_mov_b32_e32 v110, v68
	v_mov_b32_e32 v111, v69
	v_mov_b32_e32 v112, v70
	v_mov_b32_e32 v113, v71
	v_mov_b32_e32 v98, v72
	v_mov_b32_e32 v99, v73
	v_mov_b32_e32 v100, v74
	v_mov_b32_e32 v101, v75
	v_xor_b32_e32 v139, 64, v172
	v_cvt_pk_bf16_f32 v2, v228, v229
	v_cvt_pk_bf16_f32 v3, v230, v231
	v_lshlrev_b32_e32 v4, 5, v134
	v_add_u32_e32 v135, v173, v4
	v_xor_b32_e32 v5, 32, v4
	ds_write_b64 v135, v[2:3]
	v_cvt_pk_bf16_f32 v2, v232, v233
	v_cvt_pk_bf16_f32 v3, v234, v235
	v_add_u32_e32 v136, v173, v5
	v_xor_b32_e32 v5, 64, v4
	ds_write_b64 v136, v[2:3] offset:256
	v_cvt_pk_bf16_f32 v2, v236, v237
	v_cvt_pk_bf16_f32 v3, v238, v239
	v_add_u32_e32 v137, v173, v5
	v_xor_b32_e32 v4, 0x60, v4
	ds_write_b64 v137, v[2:3] offset:512
	v_cvt_pk_bf16_f32 v2, v240, v241
	v_cvt_pk_bf16_f32 v3, v242, v243
	v_add_u32_e32 v138, v173, v4
	ds_write_b64 v138, v[2:3] offset:768
	global_load_dwordx4 v[122:125], v168, s[38:39]
	global_load_dwordx4 v[118:121], v168, s[38:39] offset:2048
	global_load_dwordx4 v[126:129], v168, s[40:41]
	global_load_dwordx4 v[114:117], v168, s[40:41] offset:2048
	s_waitcnt lgkmcnt(0)
	s_barrier
	v_add_u32_e32 v2, 0x2000, v172
	s_add_i32 s71, s67, 0x2000
	v_xor_b32_e32 v140, 64, v2
	v_xor_b32_e32 v141, 32, v171
	v_xor_b32_e32 v142, 64, v171
	v_xor_b32_e32 v143, 0x60, v171
	v_xor_b32_e32 v144, 0x80, v171
	v_xor_b32_e32 v145, 0xa0, v171
	v_xor_b32_e32 v146, 0xc0, v171
	s_add_i32 s72, s67, 0x2400
	v_xor_b32_e32 v147, 0xe0, v171
	s_add_i32 s73, s67, 0x2800
	s_add_i32 s74, s67, 0x2c00
	s_add_i32 s75, s67, 0x3000
	s_add_i32 s76, s67, 0x3400
	s_mov_b32 s50, 0
	s_mov_b64 s[10:11], 0
	v_mov_b32_e32 v27, v26
	v_mov_b32_e32 v28, v26
	v_mov_b32_e32 v29, v26
	v_mov_b32_e32 v2, v26
	v_mov_b32_e32 v3, v26
	v_mov_b32_e32 v4, v26
	v_mov_b32_e32 v5, v26
	v_mov_b32_e32 v10, v26
	v_mov_b32_e32 v11, v26
	v_mov_b32_e32 v12, v26
	v_mov_b32_e32 v13, v26
	v_mov_b32_e32 v50, v26
	v_mov_b32_e32 v51, v26
	v_mov_b32_e32 v52, v26
	v_mov_b32_e32 v53, v26
	v_mov_b32_e32 v14, v26
	v_mov_b32_e32 v15, v26
	v_mov_b32_e32 v16, v26
	v_mov_b32_e32 v17, v26
	v_mov_b32_e32 v30, v26
	v_mov_b32_e32 v31, v26
	v_mov_b32_e32 v32, v26
	v_mov_b32_e32 v33, v26
	v_mov_b32_e32 v66, v26
	v_mov_b32_e32 v67, v26
	v_mov_b32_e32 v68, v26
	v_mov_b32_e32 v69, v26
	v_mov_b32_e32 v34, v26
	v_mov_b32_e32 v35, v26
	v_mov_b32_e32 v36, v26
	v_mov_b32_e32 v37, v26
	v_mov_b32_e32 v62, v26
	v_mov_b32_e32 v63, v26
	v_mov_b32_e32 v64, v26
	v_mov_b32_e32 v65, v26
	v_mov_b32_e32 v82, v26
	v_mov_b32_e32 v83, v26
	v_mov_b32_e32 v84, v26
	v_mov_b32_e32 v85, v26
	v_mov_b32_e32 v54, v26
	v_mov_b32_e32 v55, v26
	v_mov_b32_e32 v56, v26
	v_mov_b32_e32 v57, v26
	v_mov_b32_e32 v86, v26
	v_mov_b32_e32 v87, v26
	v_mov_b32_e32 v88, v26
	v_mov_b32_e32 v89, v26
	v_mov_b32_e32 v22, v26
	v_mov_b32_e32 v23, v26
	v_mov_b32_e32 v24, v26
	v_mov_b32_e32 v25, v26
	v_mov_b32_e32 v6, v26
	v_mov_b32_e32 v7, v26
	v_mov_b32_e32 v8, v26
	v_mov_b32_e32 v9, v26
	v_mov_b32_e32 v42, v26
	v_mov_b32_e32 v43, v26
	v_mov_b32_e32 v44, v26
	v_mov_b32_e32 v45, v26
	v_mov_b32_e32 v38, v26
	v_mov_b32_e32 v39, v26
	v_mov_b32_e32 v40, v26
	v_mov_b32_e32 v41, v26
	v_mov_b32_e32 v18, v26
	v_mov_b32_e32 v19, v26
	v_mov_b32_e32 v20, v26
	v_mov_b32_e32 v21, v26
	v_mov_b32_e32 v70, v26
	v_mov_b32_e32 v71, v26
	v_mov_b32_e32 v72, v26
	v_mov_b32_e32 v73, v26
	v_mov_b32_e32 v58, v26
	v_mov_b32_e32 v59, v26
	v_mov_b32_e32 v60, v26
	v_mov_b32_e32 v61, v26
	v_mov_b32_e32 v46, v26
	v_mov_b32_e32 v47, v26
	v_mov_b32_e32 v48, v26
	v_mov_b32_e32 v49, v26
	v_mov_b32_e32 v90, v26
	v_mov_b32_e32 v91, v26
	v_mov_b32_e32 v92, v26
	v_mov_b32_e32 v93, v26
	v_mov_b32_e32 v78, v26
	v_mov_b32_e32 v79, v26
	v_mov_b32_e32 v80, v26
	v_mov_b32_e32 v81, v26
	v_mov_b32_e32 v74, v26
	v_mov_b32_e32 v75, v26
	v_mov_b32_e32 v76, v26
	v_mov_b32_e32 v77, v26
	v_mov_b32_e32 v94, v26
	v_mov_b32_e32 v95, v26
	v_mov_b32_e32 v96, v26
	v_mov_b32_e32 v97, v26

.LBB0_271:
	s_mov_b32 s6, m0
	s_mov_b32 m0, s67
	s_nop 0
	global_load_lds_dwordx4 v169, s[18:19]
	s_mov_b32 m0, s6
	s_add_i32 s69, s67, 0x800
	s_mov_b32 s6, m0
	s_mov_b32 m0, s68
	s_nop 0
	global_load_lds_dwordx4 v170, s[18:19]
	s_mov_b32 m0, s6
	s_add_i32 s70, s67, 0xc00
	s_mov_b32 s6, m0
	s_mov_b32 m0, s69
	s_nop 0
	global_load_lds_dwordx4 v174, s[18:19]
	s_mov_b32 m0, s6
	v_xor_b32_e32 v102, 64, v172
	s_mov_b32 s6, m0
	s_mov_b32 m0, s70
	s_nop 0
	global_load_lds_dwordx4 v175, s[18:19]
	s_mov_b32 m0, s6
	s_waitcnt vmcnt(8)
	v_mov_b32_e32 v38, v60
	v_mov_b32_e32 v39, v61
	v_mov_b32_e32 v40, v62
	v_mov_b32_e32 v41, v63
	v_mov_b32_e32 v26, v64
	v_mov_b32_e32 v27, v65
	v_mov_b32_e32 v28, v66
	v_mov_b32_e32 v29, v67
	v_mov_b32_e32 v50, v68
	v_mov_b32_e32 v51, v69
	v_mov_b32_e32 v52, v70
	v_mov_b32_e32 v53, v71
	v_mov_b32_e32 v22, v72
	v_mov_b32_e32 v23, v73
	v_mov_b32_e32 v24, v74
	v_mov_b32_e32 v25, v75
	s_add_i32 s71, s67, 0x2000
	v_cvt_pk_bf16_f32 v2, v228, v229
	v_cvt_pk_bf16_f32 v3, v230, v231
	v_lshlrev_b32_e32 v4, 5, v134
	v_add_u32_e32 v98, v173, v4
	v_xor_b32_e32 v5, 32, v4
	ds_write_b64 v98, v[2:3]
	v_cvt_pk_bf16_f32 v2, v232, v233
	v_cvt_pk_bf16_f32 v3, v234, v235
	v_add_u32_e32 v99, v173, v5
	v_xor_b32_e32 v5, 64, v4
	ds_write_b64 v99, v[2:3] offset:256
	v_cvt_pk_bf16_f32 v2, v236, v237
	v_cvt_pk_bf16_f32 v3, v238, v239
	v_add_u32_e32 v100, v173, v5
	v_xor_b32_e32 v4, 0x60, v4
	ds_write_b64 v100, v[2:3] offset:512
	v_cvt_pk_bf16_f32 v2, v240, v241
	v_cvt_pk_bf16_f32 v3, v242, v243
	v_add_u32_e32 v101, v173, v4
	ds_write_b64 v101, v[2:3] offset:768
	global_load_dwordx4 v[78:81], v168, s[38:39]
	global_load_dwordx4 v[66:69], v168, s[38:39] offset:2048
	global_load_dwordx4 v[82:85], v168, s[40:41]
	global_load_dwordx4 v[58:61], v168, s[40:41] offset:2048
	s_waitcnt lgkmcnt(0)
	s_barrier
	v_add_u32_e32 v2, 0x2000, v172
	v_xor_b32_e32 v103, 64, v2
	v_mov_b32_e32 v2, 0
	v_xor_b32_e32 v104, 32, v171
	v_xor_b32_e32 v105, 64, v171
	v_xor_b32_e32 v106, 0x60, v171
	v_xor_b32_e32 v107, 0x80, v171
	v_xor_b32_e32 v108, 0xa0, v171
	v_xor_b32_e32 v109, 0xc0, v171
	s_add_i32 s72, s67, 0x2400
	v_xor_b32_e32 v110, 0xe0, v171
	s_add_i32 s73, s67, 0x2800
	s_add_i32 s74, s67, 0x2c00
	s_mov_b32 s52, 0
	s_mov_b64 s[48:49], 0
	v_mov_b32_e32 v3, v2
	v_mov_b32_e32 v4, v2
	v_mov_b32_e32 v5, v2
	v_mov_b32_e32 v10, v2
	v_mov_b32_e32 v11, v2
	v_mov_b32_e32 v12, v2
	v_mov_b32_e32 v13, v2
	v_mov_b32_e32 v14, v2
	v_mov_b32_e32 v15, v2
	v_mov_b32_e32 v16, v2
	v_mov_b32_e32 v17, v2
	v_mov_b32_e32 v30, v2
	v_mov_b32_e32 v31, v2
	v_mov_b32_e32 v32, v2
	v_mov_b32_e32 v33, v2
	v_mov_b32_e32 v34, v2
	v_mov_b32_e32 v35, v2
	v_mov_b32_e32 v36, v2
	v_mov_b32_e32 v37, v2
	v_mov_b32_e32 v62, v2
	v_mov_b32_e32 v63, v2
	v_mov_b32_e32 v64, v2
	v_mov_b32_e32 v65, v2
	v_mov_b32_e32 v54, v2
	v_mov_b32_e32 v55, v2
	v_mov_b32_e32 v56, v2
	v_mov_b32_e32 v57, v2
	v_mov_b32_e32 v86, v2
	v_mov_b32_e32 v87, v2
	v_mov_b32_e32 v88, v2
	v_mov_b32_e32 v89, v2
	v_mov_b32_e32 v6, v2
	v_mov_b32_e32 v7, v2
	v_mov_b32_e32 v8, v2
	v_mov_b32_e32 v9, v2
	v_mov_b32_e32 v42, v2
	v_mov_b32_e32 v43, v2
	v_mov_b32_e32 v44, v2
	v_mov_b32_e32 v45, v2
	v_mov_b32_e32 v18, v2
	v_mov_b32_e32 v19, v2
	v_mov_b32_e32 v20, v2
	v_mov_b32_e32 v21, v2
	v_mov_b32_e32 v70, v2
	v_mov_b32_e32 v71, v2
	v_mov_b32_e32 v72, v2
	v_mov_b32_e32 v73, v2
	v_mov_b32_e32 v46, v2
	v_mov_b32_e32 v47, v2
	v_mov_b32_e32 v48, v2
	v_mov_b32_e32 v49, v2
	v_mov_b32_e32 v90, v2
	v_mov_b32_e32 v91, v2
	v_mov_b32_e32 v92, v2
	v_mov_b32_e32 v93, v2
	v_mov_b32_e32 v74, v2
	v_mov_b32_e32 v75, v2
	v_mov_b32_e32 v76, v2
	v_mov_b32_e32 v77, v2
	v_mov_b32_e32 v94, v2
	v_mov_b32_e32 v95, v2
	v_mov_b32_e32 v96, v2
	v_mov_b32_e32 v97, v2

.LBB0_277:
	v_mov_b32_e32 v125, 0
	v_lshlrev_b32_e32 v98, 5, v134
	v_add_u32_e32 v99, 0x2000, v172
	s_andn2_b64 vcc, exec, s[10:11]
	v_xor_b32_e32 v178, 64, v172
	v_xor_b32_e32 v179, 32, v171
	v_xor_b32_e32 v180, 64, v171
	v_xor_b32_e32 v181, 0x60, v171
	v_xor_b32_e32 v182, 0x80, v171
	v_xor_b32_e32 v183, 0xa0, v171
	v_xor_b32_e32 v184, 0xc0, v171
	v_xor_b32_e32 v185, 0xe0, v171
	v_add_u32_e32 v186, v173, v98
	v_xor_b32_e32 v190, 32, v98
	v_xor_b32_e32 v189, 64, v98
	v_xor_b32_e32 v188, 0x60, v98
	v_xor_b32_e32 v187, 64, v99
	v_mov_b32_e32 v124, v125
	v_mov_b32_e32 v123, v125
	v_mov_b32_e32 v122, v125
	v_mov_b32_e32 v117, v125
	v_mov_b32_e32 v116, v125
	v_mov_b32_e32 v115, v125
	v_mov_b32_e32 v114, v125
	v_mov_b32_e32 v109, v125
	v_mov_b32_e32 v108, v125
	v_mov_b32_e32 v107, v125
	v_mov_b32_e32 v106, v125
	v_mov_b32_e32 v105, v125
	v_mov_b32_e32 v104, v125
	v_mov_b32_e32 v103, v125
	v_mov_b32_e32 v102, v125
	v_mov_b32_e32 v129, v125
	v_mov_b32_e32 v128, v125
	v_mov_b32_e32 v127, v125
	v_mov_b32_e32 v126, v125
	v_mov_b32_e32 v121, v125
	v_mov_b32_e32 v120, v125
	v_mov_b32_e32 v119, v125
	v_mov_b32_e32 v118, v125
	v_mov_b32_e32 v113, v125
	v_mov_b32_e32 v112, v125
	v_mov_b32_e32 v111, v125
	v_mov_b32_e32 v110, v125
	v_mov_b32_e32 v101, v125
	v_mov_b32_e32 v100, v125
	v_mov_b32_e32 v99, v125
	v_mov_b32_e32 v98, v125
	s_cbranch_vccnz .LBB0_281
	s_waitcnt vmcnt(13)
	v_lshlrev_b32_e32 v2, 8, v131
	v_and_or_b32 v191, v2, s60, v133
	s_waitcnt vmcnt(12)
	v_lshlrev_b32_e32 v2, 8, v130
	v_and_or_b32 v192, v2, s60, v132
	s_mov_b32 s6, m0
	s_mov_b32 m0, s67
	s_nop 0
	global_load_lds_dwordx4 v169, s[18:19]
	s_mov_b32 m0, s6
	s_add_i32 s50, s67, 0x800
	s_mov_b32 s6, m0
	s_mov_b32 m0, s68
	s_nop 0
	global_load_lds_dwordx4 v170, s[18:19]
	s_mov_b32 m0, s6
	s_add_i32 s51, s67, 0xc00
	s_mov_b32 s6, m0
	s_mov_b32 m0, s50
	s_nop 0
	global_load_lds_dwordx4 v174, s[18:19]
	s_mov_b32 m0, s6
	s_add_i32 s52, s67, 0x1000
	s_mov_b32 s6, m0
	s_mov_b32 m0, s51
	s_nop 0
	global_load_lds_dwordx4 v175, s[18:19]
	s_mov_b32 m0, s6
	s_add_i32 s53, s67, 0x1400
	s_mov_b32 s6, m0
	s_mov_b32 m0, s52
	s_nop 0
	global_load_lds_dwordx4 v176, s[18:19]
	s_mov_b32 m0, s6
	s_add_i32 s69, s67, 0x1800
	s_mov_b32 s6, m0
	s_mov_b32 m0, s53
	s_nop 0
	global_load_lds_dwordx4 v177, s[18:19]
	s_mov_b32 m0, s6
	s_add_i32 s70, s67, 0x1c00
	s_mov_b32 s6, m0
	s_mov_b32 m0, s69
	s_nop 0
	global_load_lds_dwordx4 v191, s[18:19]
	s_mov_b32 m0, s6
	v_add_u32_e32 v193, v173, v190
	s_mov_b32 s6, m0
	s_mov_b32 m0, s70
	s_nop 0
	global_load_lds_dwordx4 v192, s[18:19]
	s_mov_b32 m0, s6
	s_waitcnt vmcnt(12)
	v_mov_b32_e32 v138, v60
	v_mov_b32_e32 v139, v61
	v_mov_b32_e32 v140, v62
	v_mov_b32_e32 v141, v63
	v_mov_b32_e32 v134, v64
	v_mov_b32_e32 v135, v65
	v_mov_b32_e32 v136, v66
	v_mov_b32_e32 v137, v67
	v_mov_b32_e32 v142, v68
	v_mov_b32_e32 v143, v69
	v_mov_b32_e32 v144, v70
	v_mov_b32_e32 v145, v71
	v_mov_b32_e32 v130, v72
	v_mov_b32_e32 v131, v73
	v_mov_b32_e32 v132, v74
	v_mov_b32_e32 v133, v75
	v_add_u32_e32 v194, v173, v189
	v_cvt_pk_bf16_f32 v2, v228, v229
	v_cvt_pk_bf16_f32 v3, v230, v231
	ds_write_b64 v186, v[2:3]
	v_cvt_pk_bf16_f32 v2, v232, v233
	v_cvt_pk_bf16_f32 v3, v234, v235
	ds_write_b64 v193, v[2:3] offset:256
	v_cvt_pk_bf16_f32 v2, v236, v237
	v_cvt_pk_bf16_f32 v3, v238, v239
	ds_write_b64 v194, v[2:3] offset:512
	v_cvt_pk_bf16_f32 v2, v240, v241
	v_cvt_pk_bf16_f32 v3, v242, v243
	v_add_u32_e32 v195, v173, v188
	ds_write_b64 v195, v[2:3] offset:768
	global_load_dwordx4 v[154:157], v168, s[38:39]
	global_load_dwordx4 v[150:153], v168, s[38:39] offset:2048
	global_load_dwordx4 v[158:161], v168, s[40:41]
	global_load_dwordx4 v[146:149], v168, s[40:41] offset:2048
	s_waitcnt lgkmcnt(0)
	s_barrier
	v_mov_b32_e32 v98, 0
	s_add_i32 s71, s67, 0x2000
	s_add_i32 s72, s67, 0x2400
	s_add_i32 s73, s67, 0x2800
	s_add_i32 s74, s67, 0x2c00
	s_add_i32 s75, s67, 0x3000
	s_add_i32 s76, s67, 0x3400
	s_add_i32 s77, s67, 0x3800
	s_add_i32 s78, s67, 0x3c00
	s_mov_b32 s48, 0
	s_mov_b64 s[8:9], 0
	v_mov_b32_e32 v99, v98
	v_mov_b32_e32 v100, v98
	v_mov_b32_e32 v101, v98
	v_mov_b32_e32 v26, v98
	v_mov_b32_e32 v27, v98
	v_mov_b32_e32 v28, v98
	v_mov_b32_e32 v29, v98
	v_mov_b32_e32 v2, v98
	v_mov_b32_e32 v3, v98
	v_mov_b32_e32 v4, v98
	v_mov_b32_e32 v5, v98
	v_mov_b32_e32 v10, v98
	v_mov_b32_e32 v11, v98
	v_mov_b32_e32 v12, v98
	v_mov_b32_e32 v13, v98
	v_mov_b32_e32 v110, v98
	v_mov_b32_e32 v111, v98
	v_mov_b32_e32 v112, v98
	v_mov_b32_e32 v113, v98
	v_mov_b32_e32 v50, v98
	v_mov_b32_e32 v51, v98
	v_mov_b32_e32 v52, v98
	v_mov_b32_e32 v53, v98
	v_mov_b32_e32 v14, v98
	v_mov_b32_e32 v15, v98
	v_mov_b32_e32 v16, v98
	v_mov_b32_e32 v17, v98
	v_mov_b32_e32 v30, v98
	v_mov_b32_e32 v31, v98
	v_mov_b32_e32 v32, v98
	v_mov_b32_e32 v33, v98
	v_mov_b32_e32 v118, v98
	v_mov_b32_e32 v119, v98
	v_mov_b32_e32 v120, v98
	v_mov_b32_e32 v121, v98
	v_mov_b32_e32 v66, v98
	v_mov_b32_e32 v67, v98
	v_mov_b32_e32 v68, v98
	v_mov_b32_e32 v69, v98
	v_mov_b32_e32 v34, v98
	v_mov_b32_e32 v35, v98
	v_mov_b32_e32 v36, v98
	v_mov_b32_e32 v37, v98
	v_mov_b32_e32 v62, v98
	v_mov_b32_e32 v63, v98
	v_mov_b32_e32 v64, v98
	v_mov_b32_e32 v65, v98
	v_mov_b32_e32 v126, v98
	v_mov_b32_e32 v127, v98
	v_mov_b32_e32 v128, v98
	v_mov_b32_e32 v129, v98
	v_mov_b32_e32 v82, v98
	v_mov_b32_e32 v83, v98
	v_mov_b32_e32 v84, v98
	v_mov_b32_e32 v85, v98
	v_mov_b32_e32 v54, v98
	v_mov_b32_e32 v55, v98
	v_mov_b32_e32 v56, v98
	v_mov_b32_e32 v57, v98
	v_mov_b32_e32 v86, v98
	v_mov_b32_e32 v87, v98
	v_mov_b32_e32 v88, v98
	v_mov_b32_e32 v89, v98
	v_mov_b32_e32 v102, v98
	v_mov_b32_e32 v103, v98
	v_mov_b32_e32 v104, v98
	v_mov_b32_e32 v105, v98
	v_mov_b32_e32 v22, v98
	v_mov_b32_e32 v23, v98
	v_mov_b32_e32 v24, v98
	v_mov_b32_e32 v25, v98
	v_mov_b32_e32 v6, v98
	v_mov_b32_e32 v7, v98
	v_mov_b32_e32 v8, v98
	v_mov_b32_e32 v9, v98
	v_mov_b32_e32 v42, v98
	v_mov_b32_e32 v43, v98
	v_mov_b32_e32 v44, v98
	v_mov_b32_e32 v45, v98
	v_mov_b32_e32 v106, v98
	v_mov_b32_e32 v107, v98
	v_mov_b32_e32 v108, v98
	v_mov_b32_e32 v109, v98
	v_mov_b32_e32 v38, v98
	v_mov_b32_e32 v39, v98
	v_mov_b32_e32 v40, v98
	v_mov_b32_e32 v41, v98
	v_mov_b32_e32 v18, v98
	v_mov_b32_e32 v19, v98
	v_mov_b32_e32 v20, v98
	v_mov_b32_e32 v21, v98
	v_mov_b32_e32 v70, v98
	v_mov_b32_e32 v71, v98
	v_mov_b32_e32 v72, v98
	v_mov_b32_e32 v73, v98
	v_mov_b32_e32 v114, v98
	v_mov_b32_e32 v115, v98
	v_mov_b32_e32 v116, v98
	v_mov_b32_e32 v117, v98
	v_mov_b32_e32 v58, v98
	v_mov_b32_e32 v59, v98
	v_mov_b32_e32 v60, v98
	v_mov_b32_e32 v61, v98
	v_mov_b32_e32 v46, v98
	v_mov_b32_e32 v47, v98
	v_mov_b32_e32 v48, v98
	v_mov_b32_e32 v49, v98
	v_mov_b32_e32 v90, v98
	v_mov_b32_e32 v91, v98
	v_mov_b32_e32 v92, v98
	v_mov_b32_e32 v93, v98
	v_mov_b32_e32 v122, v98
	v_mov_b32_e32 v123, v98
	v_mov_b32_e32 v124, v98
	v_mov_b32_e32 v125, v98
	v_mov_b32_e32 v78, v98
	v_mov_b32_e32 v79, v98
	v_mov_b32_e32 v80, v98
	v_mov_b32_e32 v81, v98
	v_mov_b32_e32 v74, v98
	v_mov_b32_e32 v75, v98
	v_mov_b32_e32 v76, v98
	v_mov_b32_e32 v77, v98
	v_mov_b32_e32 v94, v98
	v_mov_b32_e32 v95, v98
	v_mov_b32_e32 v96, v98
	v_mov_b32_e32 v97, v98

.LBB0_281:
	s_and_b64 vcc, exec, s[8:9]
	s_cbranch_vccz .LBB0_285
	s_mov_b32 s6, m0
	s_mov_b32 m0, s67
	s_nop 0
	global_load_lds_dwordx4 v169, s[18:19]
	s_mov_b32 m0, s6
	v_add_u32_e32 v47, v173, v189
	s_mov_b32 s6, m0
	s_mov_b32 m0, s68
	s_nop 0
	global_load_lds_dwordx4 v170, s[18:19]
	s_mov_b32 m0, s6
	s_waitcnt vmcnt(6)
	v_mov_b32_e32 v18, v60
	v_mov_b32_e32 v19, v61
	v_mov_b32_e32 v20, v62
	v_mov_b32_e32 v21, v63
	v_mov_b32_e32 v6, v64
	v_mov_b32_e32 v7, v65
	v_mov_b32_e32 v8, v66
	v_mov_b32_e32 v9, v67
	v_mov_b32_e32 v14, v68
	v_mov_b32_e32 v15, v69
	v_mov_b32_e32 v16, v70
	v_mov_b32_e32 v17, v71
	v_mov_b32_e32 v2, v72
	v_mov_b32_e32 v3, v73
	v_mov_b32_e32 v4, v74
	v_mov_b32_e32 v5, v75
	v_add_u32_e32 v46, v173, v190
	v_cvt_pk_bf16_f32 v10, v228, v229
	v_cvt_pk_bf16_f32 v11, v230, v231
	ds_write_b64 v186, v[10:11]
	v_cvt_pk_bf16_f32 v10, v236, v237
	v_cvt_pk_bf16_f32 v11, v238, v239
	v_cvt_pk_bf16_f32 v12, v232, v233
	v_cvt_pk_bf16_f32 v13, v234, v235
	ds_write_b64 v47, v[10:11] offset:512
	v_cvt_pk_bf16_f32 v10, v240, v241
	v_cvt_pk_bf16_f32 v11, v242, v243
	v_add_u32_e32 v48, v173, v188
	ds_write_b64 v46, v[12:13] offset:256
	ds_write_b64 v48, v[10:11] offset:768
	global_load_dwordx4 v[38:41], v168, s[38:39]
	global_load_dwordx4 v[26:29], v168, s[38:39] offset:2048
	global_load_dwordx4 v[34:37], v168, s[40:41]
	global_load_dwordx4 v[22:25], v168, s[40:41] offset:2048
	s_waitcnt lgkmcnt(0)
	s_barrier
	v_mov_b32_e32 v10, 0
	s_add_i32 s48, s67, 0x2000
	s_add_i32 s49, s67, 0x2400
	s_mov_b32 s50, 0
	s_mov_b64 s[8:9], 0
	v_mov_b32_e32 v11, v10
	v_mov_b32_e32 v12, v10
	v_mov_b32_e32 v13, v10
	v_mov_b32_e32 v30, v10
	v_mov_b32_e32 v31, v10
	v_mov_b32_e32 v32, v10
	v_mov_b32_e32 v33, v10
	v_mov_b32_e32 v62, v10
	v_mov_b32_e32 v63, v10
	v_mov_b32_e32 v64, v10
	v_mov_b32_e32 v65, v10
	v_mov_b32_e32 v86, v10
	v_mov_b32_e32 v87, v10
	v_mov_b32_e32 v88, v10
	v_mov_b32_e32 v89, v10
	v_mov_b32_e32 v42, v10
	v_mov_b32_e32 v43, v10
	v_mov_b32_e32 v44, v10
	v_mov_b32_e32 v45, v10
	v_mov_b32_e32 v70, v10
	v_mov_b32_e32 v71, v10
	v_mov_b32_e32 v72, v10
	v_mov_b32_e32 v73, v10
	v_mov_b32_e32 v90, v10
	v_mov_b32_e32 v91, v10
	v_mov_b32_e32 v92, v10
	v_mov_b32_e32 v93, v10
	v_mov_b32_e32 v94, v10
	v_mov_b32_e32 v95, v10
	v_mov_b32_e32 v96, v10
	v_mov_b32_e32 v97, v10

.LBB0_285:
	s_nop 0
	v_readfirstlane_b32 s6, v162
	s_ashr_i32 s6, s6, 6
	s_mul_i32 s66, s66, s6
	s_waitcnt vmcnt(1)
	v_and_or_b32 v131, v162, 15, s64
	s_waitcnt vmcnt(0)
	v_lshrrev_b32_e32 v130, 2, v162
	s_lshl_b32 s50, s66, 4
	v_and_b32_e32 v130, 12, v130
	v_add_u32_e32 v132, s50, v131
	v_cmp_gt_i32_e32 vcc, s65, v132
	v_lshlrev_b32_e32 v162, 1, v130
	s_and_saveexec_b64 s[48:49], vcc
	s_cbranch_execz .LBB0_287
	v_ashrrev_i32_e32 v133, 31, v132
	v_lshl_add_u64 v[134:135], v[132:133], 2, s[26:27]
	v_mul_f32_e32 v134, 0xbfb8aa3b, v94
	v_mul_f32_e32 v135, 0xbfb8aa3b, v95
	v_exp_f32_e32 v134, v134
	v_exp_f32_e32 v135, v135
	v_mul_f32_e32 v136, 0xbfb8aa3b, v96
	v_mul_f32_e32 v137, 0xbfb8aa3b, v97
	v_exp_f32_e32 v136, v136
	v_exp_f32_e32 v137, v137
	v_pk_add_f32 v[134:135], v[134:135], 1.0 op_sel_hi:[1,0]
	v_mul_f32_e32 v138, 0xbfb8aa3b, v90
	v_pk_add_f32 v[136:137], v[136:137], 1.0 op_sel_hi:[1,0]
	v_mul_f32_e32 v139, 0xbfb8aa3b, v91
	v_exp_f32_e32 v138, v138
	v_exp_f32_e32 v139, v139
	v_rcp_f32_e32 v140, v135
	s_nop 0
	v_mul_f32_e32 v95, v95, v140
	v_rcp_f32_e32 v135, v134
	s_nop 0
	v_mul_f32_e32 v94, v94, v135
	v_pk_mul_f32 v[86:87], v[86:87], v[94:95]
	v_pk_add_f32 v[138:139], v[138:139], 1.0 op_sel_hi:[1,0]
	v_rcp_f32_e32 v134, v137
	s_nop 0
	v_mul_f32_e32 v95, v97, v134
	v_rcp_f32_e32 v94, v136
	s_nop 0
	v_mul_f32_e32 v94, v96, v94
	v_add_u32_e32 v132, s63, v132
	v_pk_mul_f32 v[88:89], v[88:89], v[94:95]
	v_ashrrev_i32_e32 v133, 31, v132
	v_lshlrev_b64 v[132:133], 9, v[132:133]
	v_lshl_add_u64 v[132:133], s[20:21], 0, v[132:133]
	v_mov_b32_e32 v130, v244
	v_pk_mul_f32 v[86:87], v[86:87], v[130:131] op_sel_hi:[1,0]
	v_pk_mul_f32 v[88:89], v[88:89], v[130:131] op_sel_hi:[1,0]
	v_lshl_add_u64 v[132:133], v[132:133], 0, v[162:163]
	v_cvt_pk_bf16_f32 v86, v86, v87
	v_cvt_pk_bf16_f32 v87, v88, v89
	global_store_dwordx2 v[132:133], v[86:87], off
	v_rcp_f32_e32 v86, v139
	s_nop 0
	v_mul_f32_e32 v87, v91, v86
	v_mul_f32_e32 v88, 0xbfb8aa3b, v92
	v_mul_f32_e32 v89, 0xbfb8aa3b, v93
	v_exp_f32_e32 v88, v88
	v_exp_f32_e32 v89, v89
	v_rcp_f32_e32 v86, v138
	s_nop 0
	v_mul_f32_e32 v86, v90, v86
	v_pk_mul_f32 v[62:63], v[62:63], v[86:87]
	v_pk_add_f32 v[88:89], v[88:89], 1.0 op_sel_hi:[1,0]
	v_pk_mul_f32 v[62:63], v[62:63], v[130:131] op_sel_hi:[1,0]
	v_cvt_pk_bf16_f32 v62, v62, v63
	v_rcp_f32_e32 v63, v89
	s_nop 0
	v_mul_f32_e32 v87, v93, v63
	v_mul_f32_e32 v89, 0xbfb8aa3b, v70
	v_exp_f32_e32 v90, v89
	v_mul_f32_e32 v89, 0xbfb8aa3b, v71
	v_exp_f32_e32 v91, v89
	v_rcp_f32_e32 v63, v88
	s_nop 0
	v_mul_f32_e32 v86, v92, v63
	v_pk_mul_f32 v[64:65], v[64:65], v[86:87]
	v_pk_add_f32 v[86:87], v[90:91], 1.0 op_sel_hi:[1,0]
	v_pk_mul_f32 v[64:65], v[64:65], v[130:131] op_sel_hi:[1,0]
	v_cvt_pk_bf16_f32 v63, v64, v65
	global_store_dwordx2 v[132:133], v[62:63], off offset:32
	v_rcp_f32_e32 v62, v87
	s_nop 0
	v_mul_f32_e32 v63, v71, v62
	v_mul_f32_e32 v64, 0xbfb8aa3b, v72
	v_mul_f32_e32 v65, 0xbfb8aa3b, v73
	v_exp_f32_e32 v64, v64
	v_exp_f32_e32 v65, v65
	v_rcp_f32_e32 v62, v86
	s_nop 0
	v_mul_f32_e32 v62, v70, v62
	v_pk_mul_f32 v[30:31], v[30:31], v[62:63]
	v_pk_add_f32 v[64:65], v[64:65], 1.0 op_sel_hi:[1,0]
	v_pk_mul_f32 v[30:31], v[30:31], v[130:131] op_sel_hi:[1,0]
	v_cvt_pk_bf16_f32 v30, v30, v31
	v_rcp_f32_e32 v31, v65
	s_nop 0
	v_mul_f32_e32 v63, v73, v31
	v_mul_f32_e32 v65, 0xbfb8aa3b, v42
	v_exp_f32_e32 v70, v65
	v_mul_f32_e32 v65, 0xbfb8aa3b, v43
	v_exp_f32_e32 v71, v65
	v_rcp_f32_e32 v31, v64
	s_nop 0
	v_mul_f32_e32 v62, v72, v31
	v_pk_mul_f32 v[32:33], v[32:33], v[62:63]
	v_pk_add_f32 v[62:63], v[70:71], 1.0 op_sel_hi:[1,0]
	v_pk_mul_f32 v[32:33], v[32:33], v[130:131] op_sel_hi:[1,0]
	v_cvt_pk_bf16_f32 v31, v32, v33
	global_store_dwordx2 v[132:133], v[30:31], off offset:64
	v_rcp_f32_e32 v30, v63
	s_nop 0
	v_mul_f32_e32 v31, v43, v30
	v_mul_f32_e32 v32, 0xbfb8aa3b, v44
	v_mul_f32_e32 v33, 0xbfb8aa3b, v45
	v_exp_f32_e32 v32, v32
	v_exp_f32_e32 v33, v33
	v_rcp_f32_e32 v30, v62
	s_nop 0
	v_mul_f32_e32 v30, v42, v30
	v_pk_mul_f32 v[10:11], v[10:11], v[30:31]
	v_pk_add_f32 v[32:33], v[32:33], 1.0 op_sel_hi:[1,0]
	v_pk_mul_f32 v[10:11], v[10:11], v[130:131] op_sel_hi:[1,0]
	v_cvt_pk_bf16_f32 v10, v10, v11
	v_rcp_f32_e32 v11, v33
	s_nop 0
	v_mul_f32_e32 v31, v45, v11
	v_rcp_f32_e32 v11, v32
	s_nop 0
	v_mul_f32_e32 v30, v44, v11
	v_pk_mul_f32 v[12:13], v[12:13], v[30:31]
	s_nop 0
	v_pk_mul_f32 v[12:13], v[12:13], v[130:131] op_sel_hi:[1,0]
	s_nop 0
	v_cvt_pk_bf16_f32 v11, v12, v13
	global_store_dwordx2 v[132:133], v[10:11], off offset:96
.LBB0_287:
	s_or_b64 exec, exec, s[48:49]
	v_or_b32_e32 v10, 16, v131
	v_add_u32_e32 v12, s50, v10
	v_cmp_gt_i32_e32 vcc, s65, v12
	s_and_b64 s[6:7], s[46:47], vcc
	s_and_saveexec_b64 s[46:47], s[6:7]
	s_cbranch_execz .LBB0_289
	v_ashrrev_i32_e32 v13, 31, v12
	v_lshl_add_u64 v[10:11], v[12:13], 2, s[26:27]
	v_mul_f32_e32 v11, 0xbfb8aa3b, v74
	v_mul_f32_e32 v31, 0xbfb8aa3b, v75
	v_exp_f32_e32 v30, v11
	v_exp_f32_e32 v31, v31
	v_mul_f32_e32 v32, 0xbfb8aa3b, v76
	v_mul_f32_e32 v33, 0xbfb8aa3b, v77
	v_exp_f32_e32 v32, v32
	v_exp_f32_e32 v33, v33
	v_pk_add_f32 v[30:31], v[30:31], 1.0 op_sel_hi:[1,0]
	v_mul_f32_e32 v42, 0xbfb8aa3b, v46
	v_pk_add_f32 v[32:33], v[32:33], 1.0 op_sel_hi:[1,0]
	v_mul_f32_e32 v43, 0xbfb8aa3b, v47
	v_exp_f32_e32 v42, v42
	v_exp_f32_e32 v43, v43
	v_rcp_f32_e32 v11, v31
	s_nop 0
	v_mul_f32_e32 v31, v75, v11
	v_rcp_f32_e32 v11, v30
	s_nop 0
	v_mul_f32_e32 v30, v74, v11
	v_pk_add_f32 v[42:43], v[42:43], 1.0 op_sel_hi:[1,0]
	v_pk_mul_f32 v[30:31], v[54:55], v[30:31]
	v_rcp_f32_e32 v11, v33
	s_nop 0
	v_mul_f32_e32 v33, v77, v11
	v_add_u32_e32 v12, s63, v12
	v_rcp_f32_e32 v11, v32
	s_nop 0
	v_mul_f32_e32 v32, v76, v11
	v_ashrrev_i32_e32 v13, 31, v12
	v_lshlrev_b64 v[12:13], 9, v[12:13]
	v_pk_mul_f32 v[32:33], v[56:57], v[32:33]
	v_lshl_add_u64 v[12:13], s[20:21], 0, v[12:13]
	v_lshl_add_u64 v[12:13], v[12:13], 0, v[162:163]
	v_mov_b32_e32 v10, v245
	v_pk_mul_f32 v[30:31], v[30:31], v[10:11] op_sel_hi:[1,0]
	v_pk_mul_f32 v[32:33], v[32:33], v[10:11] op_sel_hi:[1,0]
	v_cvt_pk_bf16_f32 v30, v30, v31
	v_cvt_pk_bf16_f32 v31, v32, v33
	global_store_dwordx2 v[12:13], v[30:31], off
	v_rcp_f32_e32 v11, v43
	s_nop 0
	v_mul_f32_e32 v31, v47, v11
	v_mul_f32_e32 v30, 0xbfb8aa3b, v48
	v_exp_f32_e32 v32, v30
	v_mul_f32_e32 v30, 0xbfb8aa3b, v49
	v_exp_f32_e32 v33, v30
	v_rcp_f32_e32 v11, v42
	s_nop 0
	v_mul_f32_e32 v30, v46, v11
	v_pk_mul_f32 v[30:31], v[34:35], v[30:31]
	v_pk_add_f32 v[32:33], v[32:33], 1.0 op_sel_hi:[1,0]
	s_nop 0
	v_pk_mul_f32 v[30:31], v[30:31], v[10:11] op_sel_hi:[1,0]
	s_nop 0
	v_cvt_pk_bf16_f32 v30, v30, v31
	v_rcp_f32_e32 v11, v33
	s_nop 0
	v_mul_f32_e32 v33, v49, v11
	v_mul_f32_e32 v31, 0xbfb8aa3b, v18
	v_exp_f32_e32 v34, v31
	v_mul_f32_e32 v31, 0xbfb8aa3b, v19
	v_exp_f32_e32 v35, v31
	v_rcp_f32_e32 v11, v32
	s_nop 0
	v_mul_f32_e32 v32, v48, v11
	v_pk_mul_f32 v[32:33], v[36:37], v[32:33]
	v_pk_add_f32 v[34:35], v[34:35], 1.0 op_sel_hi:[1,0]
	s_nop 0
	v_pk_mul_f32 v[32:33], v[32:33], v[10:11] op_sel_hi:[1,0]
	s_nop 0
	v_cvt_pk_bf16_f32 v31, v32, v33
	global_store_dwordx2 v[12:13], v[30:31], off offset:32
	v_rcp_f32_e32 v11, v35
	s_nop 0
	v_mul_f32_e32 v19, v19, v11
	v_mul_f32_e32 v30, 0xbfb8aa3b, v20
	v_mul_f32_e32 v31, 0xbfb8aa3b, v21
	v_exp_f32_e32 v30, v30
	v_exp_f32_e32 v31, v31
	v_rcp_f32_e32 v11, v34
	s_nop 0
	v_mul_f32_e32 v18, v18, v11
	v_pk_mul_f32 v[14:15], v[14:15], v[18:19]
	v_pk_add_f32 v[30:31], v[30:31], 1.0 op_sel_hi:[1,0]
	s_nop 0
	v_pk_mul_f32 v[14:15], v[14:15], v[10:11] op_sel_hi:[1,0]
	s_nop 0
	v_cvt_pk_bf16_f32 v14, v14, v15
	v_rcp_f32_e32 v11, v31
	s_nop 0
	v_mul_f32_e32 v19, v21, v11
	v_mul_f32_e32 v15, 0xbfb8aa3b, v6
	v_exp_f32_e32 v32, v15
	v_mul_f32_e32 v15, 0xbfb8aa3b, v7
	v_exp_f32_e32 v33, v15
	v_rcp_f32_e32 v11, v30
	s_nop 0
	v_mul_f32_e32 v18, v20, v11
	v_pk_mul_f32 v[16:17], v[16:17], v[18:19]
	v_pk_add_f32 v[18:19], v[32:33], 1.0 op_sel_hi:[1,0]
	s_nop 0
	v_pk_mul_f32 v[16:17], v[16:17], v[10:11] op_sel_hi:[1,0]
	s_nop 0
	v_cvt_pk_bf16_f32 v15, v16, v17
	global_store_dwordx2 v[12:13], v[14:15], off offset:64
	v_rcp_f32_e32 v11, v19
	s_nop 0
	v_mul_f32_e32 v7, v7, v11
	v_mul_f32_e32 v14, 0xbfb8aa3b, v8
	v_mul_f32_e32 v15, 0xbfb8aa3b, v9
	v_exp_f32_e32 v14, v14
	v_exp_f32_e32 v15, v15
	v_rcp_f32_e32 v11, v18
	s_nop 0
	v_mul_f32_e32 v6, v6, v11
	v_pk_mul_f32 v[2:3], v[2:3], v[6:7]
	v_pk_add_f32 v[14:15], v[14:15], 1.0 op_sel_hi:[1,0]
	s_nop 0
	v_pk_mul_f32 v[2:3], v[2:3], v[10:11] op_sel_hi:[1,0]
	s_nop 0
	v_cvt_pk_bf16_f32 v2, v2, v3
	v_rcp_f32_e32 v3, v15
	s_nop 0
	v_mul_f32_e32 v7, v9, v3
	v_rcp_f32_e32 v3, v14
	s_nop 0
	v_mul_f32_e32 v6, v8, v3
	v_pk_mul_f32 v[4:5], v[4:5], v[6:7]
	s_nop 0
	v_pk_mul_f32 v[4:5], v[4:5], v[10:11] op_sel_hi:[1,0]
	s_nop 0
	v_cvt_pk_bf16_f32 v3, v4, v5
	global_store_dwordx2 v[12:13], v[2:3], off offset:96
.LBB0_289:
	s_or_b64 exec, exec, s[46:47]
	v_or_b32_e32 v2, 32, v131
	v_add_u32_e32 v4, s50, v2
	v_cmp_gt_i32_e32 vcc, s65, v4
	s_and_b64 s[6:7], s[44:45], vcc
	s_and_saveexec_b64 s[44:45], s[6:7]
	s_cbranch_execz .LBB0_291
	v_ashrrev_i32_e32 v5, 31, v4
	v_lshl_add_u64 v[2:3], v[4:5], 2, s[26:27]
	v_mul_f32_e32 v3, 0xbfb8aa3b, v78
	v_mul_f32_e32 v7, 0xbfb8aa3b, v79
	v_exp_f32_e32 v6, v3
	v_exp_f32_e32 v7, v7
	v_mul_f32_e32 v8, 0xbfb8aa3b, v80
	v_mul_f32_e32 v9, 0xbfb8aa3b, v81
	v_exp_f32_e32 v8, v8
	v_exp_f32_e32 v9, v9
	v_pk_add_f32 v[6:7], v[6:7], 1.0 op_sel_hi:[1,0]
	v_mul_f32_e32 v10, 0xbfb8aa3b, v58
	v_pk_add_f32 v[8:9], v[8:9], 1.0 op_sel_hi:[1,0]
	v_mul_f32_e32 v11, 0xbfb8aa3b, v59
	v_exp_f32_e32 v10, v10
	v_exp_f32_e32 v11, v11
	v_rcp_f32_e32 v3, v7
	s_nop 0
	v_mul_f32_e32 v7, v79, v3
	v_rcp_f32_e32 v3, v6
	s_nop 0
	v_mul_f32_e32 v6, v78, v3
	v_pk_add_f32 v[10:11], v[10:11], 1.0 op_sel_hi:[1,0]
	v_pk_mul_f32 v[6:7], v[82:83], v[6:7]
	v_rcp_f32_e32 v3, v9
	s_nop 0
	v_mul_f32_e32 v9, v81, v3
	v_add_u32_e32 v4, s63, v4
	v_rcp_f32_e32 v3, v8
	s_nop 0
	v_mul_f32_e32 v8, v80, v3
	v_ashrrev_i32_e32 v5, 31, v4
	v_lshlrev_b64 v[4:5], 9, v[4:5]
	v_pk_mul_f32 v[8:9], v[84:85], v[8:9]
	v_lshl_add_u64 v[4:5], s[20:21], 0, v[4:5]
	v_lshl_add_u64 v[4:5], v[4:5], 0, v[162:163]
	v_mov_b32_e32 v2, v246
	v_pk_mul_f32 v[6:7], v[6:7], v[2:3] op_sel_hi:[1,0]
	v_pk_mul_f32 v[8:9], v[8:9], v[2:3] op_sel_hi:[1,0]
	v_cvt_pk_bf16_f32 v6, v6, v7
	v_cvt_pk_bf16_f32 v7, v8, v9
	global_store_dwordx2 v[4:5], v[6:7], off
	v_rcp_f32_e32 v3, v11
	s_nop 0
	v_mul_f32_e32 v7, v59, v3
	v_mul_f32_e32 v6, 0xbfb8aa3b, v60
	v_exp_f32_e32 v8, v6
	v_mul_f32_e32 v6, 0xbfb8aa3b, v61
	v_exp_f32_e32 v9, v6
	v_rcp_f32_e32 v3, v10
	s_nop 0
	v_mul_f32_e32 v6, v58, v3
	v_pk_mul_f32 v[6:7], v[66:67], v[6:7]
	v_pk_add_f32 v[8:9], v[8:9], 1.0 op_sel_hi:[1,0]
	s_nop 0
	v_pk_mul_f32 v[6:7], v[6:7], v[2:3] op_sel_hi:[1,0]
	s_nop 0
	v_cvt_pk_bf16_f32 v6, v6, v7
	v_rcp_f32_e32 v3, v9
	s_nop 0
	v_mul_f32_e32 v9, v61, v3
	v_mul_f32_e32 v7, 0xbfb8aa3b, v38
	v_exp_f32_e32 v10, v7
	v_mul_f32_e32 v7, 0xbfb8aa3b, v39
	v_exp_f32_e32 v11, v7
	v_rcp_f32_e32 v3, v8
	s_nop 0
	v_mul_f32_e32 v8, v60, v3
	v_pk_mul_f32 v[8:9], v[68:69], v[8:9]
	v_pk_add_f32 v[10:11], v[10:11], 1.0 op_sel_hi:[1,0]
	s_nop 0
	v_pk_mul_f32 v[8:9], v[8:9], v[2:3] op_sel_hi:[1,0]
	s_nop 0
	v_cvt_pk_bf16_f32 v7, v8, v9
	global_store_dwordx2 v[4:5], v[6:7], off offset:32
	v_rcp_f32_e32 v3, v11
	s_nop 0
	v_mul_f32_e32 v7, v39, v3
	v_mul_f32_e32 v6, 0xbfb8aa3b, v40
	v_exp_f32_e32 v8, v6
	v_mul_f32_e32 v6, 0xbfb8aa3b, v41
	v_exp_f32_e32 v9, v6
	v_rcp_f32_e32 v3, v10
	s_nop 0
	v_mul_f32_e32 v6, v38, v3
	v_pk_mul_f32 v[6:7], v[50:51], v[6:7]
	v_pk_add_f32 v[8:9], v[8:9], 1.0 op_sel_hi:[1,0]
	s_nop 0
	v_pk_mul_f32 v[6:7], v[6:7], v[2:3] op_sel_hi:[1,0]
	s_nop 0
	v_cvt_pk_bf16_f32 v6, v6, v7
	v_rcp_f32_e32 v3, v9
	s_nop 0
	v_mul_f32_e32 v9, v41, v3
	v_mul_f32_e32 v7, 0xbfb8aa3b, v22
	v_exp_f32_e32 v10, v7
	v_mul_f32_e32 v7, 0xbfb8aa3b, v23
	v_exp_f32_e32 v11, v7
	v_rcp_f32_e32 v3, v8
	s_nop 0
	v_mul_f32_e32 v8, v40, v3
	v_pk_mul_f32 v[8:9], v[52:53], v[8:9]
	v_pk_add_f32 v[10:11], v[10:11], 1.0 op_sel_hi:[1,0]
	s_nop 0
	v_pk_mul_f32 v[8:9], v[8:9], v[2:3] op_sel_hi:[1,0]
	s_nop 0
	v_cvt_pk_bf16_f32 v7, v8, v9
	global_store_dwordx2 v[4:5], v[6:7], off offset:64
	v_rcp_f32_e32 v3, v11
	s_nop 0
	v_mul_f32_e32 v7, v23, v3
	v_mul_f32_e32 v6, 0xbfb8aa3b, v24
	v_exp_f32_e32 v8, v6
	v_mul_f32_e32 v6, 0xbfb8aa3b, v25
	v_exp_f32_e32 v9, v6
	v_rcp_f32_e32 v3, v10
	s_nop 0
	v_mul_f32_e32 v6, v22, v3
	v_pk_mul_f32 v[6:7], v[26:27], v[6:7]
	v_pk_add_f32 v[8:9], v[8:9], 1.0 op_sel_hi:[1,0]
	s_nop 0
	v_pk_mul_f32 v[6:7], v[6:7], v[2:3] op_sel_hi:[1,0]
	s_nop 0
	v_cvt_pk_bf16_f32 v6, v6, v7
	v_rcp_f32_e32 v3, v9
	s_nop 0
	v_mul_f32_e32 v9, v25, v3
	v_rcp_f32_e32 v3, v8
	s_nop 0
	v_mul_f32_e32 v8, v24, v3
	v_pk_mul_f32 v[8:9], v[28:29], v[8:9]
	s_nop 0
	v_pk_mul_f32 v[2:3], v[8:9], v[2:3] op_sel_hi:[1,0]
	s_nop 0
	v_cvt_pk_bf16_f32 v7, v2, v3
	global_store_dwordx2 v[4:5], v[6:7], off offset:96
.LBB0_291:
	s_or_b64 exec, exec, s[44:45]
	v_or_b32_e32 v2, 48, v131
	v_add_u32_e32 v4, s50, v2
	v_cmp_gt_i32_e32 vcc, s65, v4
	s_and_b64 s[6:7], s[42:43], vcc
	s_and_saveexec_b64 s[42:43], s[6:7]
	s_cbranch_execz .LBB0_262
	v_ashrrev_i32_e32 v5, 31, v4
	v_lshl_add_u64 v[2:3], v[4:5], 2, s[26:27]
	v_mul_f32_e32 v3, 0xbfb8aa3b, v122
	v_mul_f32_e32 v7, 0xbfb8aa3b, v123
	v_exp_f32_e32 v6, v3
	v_exp_f32_e32 v7, v7
	v_mul_f32_e32 v8, 0xbfb8aa3b, v124
	v_mul_f32_e32 v9, 0xbfb8aa3b, v125
	v_exp_f32_e32 v8, v8
	v_exp_f32_e32 v9, v9
	v_pk_add_f32 v[6:7], v[6:7], 1.0 op_sel_hi:[1,0]
	v_mul_f32_e32 v10, 0xbfb8aa3b, v114
	v_pk_add_f32 v[8:9], v[8:9], 1.0 op_sel_hi:[1,0]
	v_mul_f32_e32 v11, 0xbfb8aa3b, v115
	v_exp_f32_e32 v10, v10
	v_exp_f32_e32 v11, v11
	v_rcp_f32_e32 v3, v7
	s_nop 0
	v_mul_f32_e32 v7, v123, v3
	v_rcp_f32_e32 v3, v6
	s_nop 0
	v_mul_f32_e32 v6, v122, v3
	v_pk_add_f32 v[10:11], v[10:11], 1.0 op_sel_hi:[1,0]
	v_pk_mul_f32 v[6:7], v[126:127], v[6:7]
	v_rcp_f32_e32 v3, v9
	s_nop 0
	v_mul_f32_e32 v9, v125, v3
	v_add_u32_e32 v4, s63, v4
	v_rcp_f32_e32 v3, v8
	s_nop 0
	v_mul_f32_e32 v8, v124, v3
	v_ashrrev_i32_e32 v5, 31, v4
	v_lshlrev_b64 v[4:5], 9, v[4:5]
	v_pk_mul_f32 v[8:9], v[128:129], v[8:9]
	v_lshl_add_u64 v[4:5], s[20:21], 0, v[4:5]
	v_lshl_add_u64 v[4:5], v[4:5], 0, v[162:163]
	v_mov_b32_e32 v2, v247
	v_pk_mul_f32 v[6:7], v[6:7], v[2:3] op_sel_hi:[1,0]
	v_pk_mul_f32 v[8:9], v[8:9], v[2:3] op_sel_hi:[1,0]
	v_cvt_pk_bf16_f32 v6, v6, v7
	v_cvt_pk_bf16_f32 v7, v8, v9
	global_store_dwordx2 v[4:5], v[6:7], off
	v_rcp_f32_e32 v3, v11
	s_nop 0
	v_mul_f32_e32 v7, v115, v3
	v_mul_f32_e32 v6, 0xbfb8aa3b, v116
	v_exp_f32_e32 v8, v6
	v_mul_f32_e32 v6, 0xbfb8aa3b, v117
	v_exp_f32_e32 v9, v6
	v_rcp_f32_e32 v3, v10
	s_nop 0
	v_mul_f32_e32 v6, v114, v3
	v_pk_mul_f32 v[6:7], v[118:119], v[6:7]
	v_pk_add_f32 v[8:9], v[8:9], 1.0 op_sel_hi:[1,0]
	s_nop 0
	v_pk_mul_f32 v[6:7], v[6:7], v[2:3] op_sel_hi:[1,0]
	s_nop 0
	v_cvt_pk_bf16_f32 v6, v6, v7
	v_rcp_f32_e32 v3, v9
	s_nop 0
	v_mul_f32_e32 v9, v117, v3
	v_mul_f32_e32 v7, 0xbfb8aa3b, v106
	v_exp_f32_e32 v10, v7
	v_mul_f32_e32 v7, 0xbfb8aa3b, v107
	v_exp_f32_e32 v11, v7
	v_rcp_f32_e32 v3, v8
	s_nop 0
	v_mul_f32_e32 v8, v116, v3
	v_pk_mul_f32 v[8:9], v[120:121], v[8:9]
	v_pk_add_f32 v[10:11], v[10:11], 1.0 op_sel_hi:[1,0]
	s_nop 0
	v_pk_mul_f32 v[8:9], v[8:9], v[2:3] op_sel_hi:[1,0]
	s_nop 0
	v_cvt_pk_bf16_f32 v7, v8, v9
	global_store_dwordx2 v[4:5], v[6:7], off offset:32
	v_rcp_f32_e32 v3, v11
	s_nop 0
	v_mul_f32_e32 v7, v107, v3
	v_mul_f32_e32 v6, 0xbfb8aa3b, v108
	v_exp_f32_e32 v8, v6
	v_mul_f32_e32 v6, 0xbfb8aa3b, v109
	v_exp_f32_e32 v9, v6
	v_rcp_f32_e32 v3, v10
	s_nop 0
	v_mul_f32_e32 v6, v106, v3
	v_pk_mul_f32 v[6:7], v[110:111], v[6:7]
	v_pk_add_f32 v[8:9], v[8:9], 1.0 op_sel_hi:[1,0]
	s_nop 0
	v_pk_mul_f32 v[6:7], v[6:7], v[2:3] op_sel_hi:[1,0]
	s_nop 0
	v_cvt_pk_bf16_f32 v6, v6, v7
	v_rcp_f32_e32 v3, v9
	s_nop 0
	v_mul_f32_e32 v9, v109, v3
	v_mul_f32_e32 v7, 0xbfb8aa3b, v102
	v_exp_f32_e32 v10, v7
	v_mul_f32_e32 v7, 0xbfb8aa3b, v103
	v_exp_f32_e32 v11, v7
	v_rcp_f32_e32 v3, v8
	s_nop 0
	v_mul_f32_e32 v8, v108, v3
	v_pk_mul_f32 v[8:9], v[112:113], v[8:9]
	v_pk_add_f32 v[10:11], v[10:11], 1.0 op_sel_hi:[1,0]
	s_nop 0
	v_pk_mul_f32 v[8:9], v[8:9], v[2:3] op_sel_hi:[1,0]
	s_nop 0
	v_cvt_pk_bf16_f32 v7, v8, v9
	global_store_dwordx2 v[4:5], v[6:7], off offset:64
	v_rcp_f32_e32 v3, v11
	s_nop 0
	v_mul_f32_e32 v7, v103, v3
	v_mul_f32_e32 v6, 0xbfb8aa3b, v104
	v_exp_f32_e32 v8, v6
	v_mul_f32_e32 v6, 0xbfb8aa3b, v105
	v_exp_f32_e32 v9, v6
	v_rcp_f32_e32 v3, v10
	s_nop 0
	v_mul_f32_e32 v6, v102, v3
	v_pk_mul_f32 v[6:7], v[98:99], v[6:7]
	v_pk_add_f32 v[8:9], v[8:9], 1.0 op_sel_hi:[1,0]
	s_nop 0
	v_pk_mul_f32 v[6:7], v[6:7], v[2:3] op_sel_hi:[1,0]
	s_nop 0
	v_cvt_pk_bf16_f32 v6, v6, v7
	v_rcp_f32_e32 v3, v9
	s_nop 0
	v_mul_f32_e32 v9, v105, v3
	v_rcp_f32_e32 v3, v8
	s_nop 0
	v_mul_f32_e32 v8, v104, v3
	v_pk_mul_f32 v[8:9], v[100:101], v[8:9]
	s_nop 0
	v_pk_mul_f32 v[2:3], v[8:9], v[2:3] op_sel_hi:[1,0]
	s_nop 0
	v_cvt_pk_bf16_f32 v7, v2, v3
	global_store_dwordx2 v[4:5], v[6:7], off offset:96
	s_branch .LBB0_262

.LBB0_869:
	s_sub_i32 s11, s62, s64
	v_mov_b32_e32 v162, v0
	s_min_i32 s11, s11, 0x200
	s_add_i32 s12, s11, 0x7f
	v_readfirstlane_b32 s10, v162
	s_lshr_b32 s66, s12, 7
	s_ashr_i32 s12, s10, 2
	s_and_b32 s12, s12, -16
	s_mul_i32 s12, s12, s66
	s_add_i32 s12, s12, s64
	v_bfe_u32 v2, v162, 3, 3
	v_or_b32_e32 v10, s12, v2
	s_add_i32 s65, s11, s64
	v_mov_b32_e32 v11, s64
	v_cmp_gt_i32_e32 vcc, s65, v10
	v_or_b32_e32 v4, 8, v10
	v_add_u32_e32 v6, 16, v10
	v_cndmask_b32_e32 v2, v11, v10, vcc
	v_cmp_gt_i32_e32 vcc, s65, v4
	s_cmpk_gt_u32 s11, 0x80
	s_cselect_b64 s[44:45], -1, 0
	v_cndmask_b32_e32 v4, v11, v4, vcc
	v_cmp_gt_i32_e32 vcc, s65, v6
	s_and_b64 vcc, s[44:45], vcc
	v_add_u32_e32 v8, 24, v10
	v_cndmask_b32_e32 v6, v11, v6, vcc
	v_cmp_gt_i32_e32 vcc, s65, v8
	s_and_b64 vcc, s[44:45], vcc
	v_ashrrev_i32_e32 v3, 31, v2
	v_ashrrev_i32_e32 v7, 31, v6
	v_cndmask_b32_e32 v8, v11, v8, vcc
	v_lshl_add_u64 v[2:3], v[2:3], 2, s[24:25]
	v_ashrrev_i32_e32 v5, 31, v4
	v_lshl_add_u64 v[6:7], v[6:7], 2, s[24:25]
	v_ashrrev_i32_e32 v9, 31, v8
	v_lshl_add_u64 v[4:5], v[4:5], 2, s[24:25]
	v_lshl_add_u64 v[8:9], v[8:9], 2, s[24:25]
	global_load_dword v12, v[2:3], off
	global_load_dword v13, v[4:5], off
	s_nop 0
	global_load_dword v6, v[6:7], off
	s_nop 0
	global_load_dword v7, v[8:9], off
	v_add_u32_e32 v2, 32, v10
	s_cmpk_gt_u32 s11, 0x100
	s_cselect_b64 s[42:43], -1, 0
	v_cmp_gt_i32_e32 vcc, s65, v2
	s_and_b64 vcc, s[42:43], vcc
	v_add_u32_e32 v4, 40, v10
	v_cndmask_b32_e32 v2, v11, v2, vcc
	v_cmp_gt_i32_e32 vcc, s65, v4
	s_and_b64 vcc, s[42:43], vcc
	v_ashrrev_i32_e32 v3, 31, v2
	v_cndmask_b32_e32 v4, v11, v4, vcc
	v_lshl_add_u64 v[2:3], v[2:3], 2, s[24:25]
	v_ashrrev_i32_e32 v5, 31, v4
	v_lshl_add_u64 v[4:5], v[4:5], 2, s[24:25]
	global_load_dword v8, v[2:3], off
	global_load_dword v9, v[4:5], off
	v_add_u32_e32 v2, 48, v10
	s_cmpk_gt_u32 s11, 0x180
	s_cselect_b64 s[40:41], -1, 0
	v_cmp_gt_i32_e32 vcc, s65, v2
	s_and_b64 vcc, s[40:41], vcc
	v_add_u32_e32 v4, 56, v10
	v_cndmask_b32_e32 v2, v11, v2, vcc
	v_cmp_gt_i32_e32 vcc, s65, v4
	s_and_b64 vcc, s[40:41], vcc
	v_ashrrev_i32_e32 v3, 31, v2
	v_cndmask_b32_e32 v4, v11, v4, vcc
	v_lshl_add_u64 v[2:3], v[2:3], 2, s[24:25]
	v_ashrrev_i32_e32 v5, 31, v4
	v_lshl_add_u64 v[4:5], v[4:5], 2, s[24:25]
	global_load_dword v131, v[2:3], off
	global_load_dword v130, v[4:5], off
	v_and_b32_e32 v10, 31, v162
	v_and_b32_e32 v2, 7, v162
	v_bfe_u32 v3, v162, 4, 2
	v_cmp_gt_u32_e32 vcc, 16, v10
	v_bitop3_b32 v2, v3, v2, 4 bitop3:0x36
	v_ashrrev_i32_e32 v11, 5, v162
	v_cndmask_b32_e32 v15, v166, v167, vcc
	v_bitop3_b32 v14, v3, v162, 7 bitop3:0x78
	v_lshlrev_b32_e32 v132, 4, v2
	v_lshl_add_u32 v2, v10, 4, v15
	v_lshlrev_b32_e32 v133, 4, v14
	v_lshl_or_b32 v168, v11, 13, v2
	global_load_dwordx4 v[228:231], v168, s[22:23]
	global_load_dwordx4 v[232:235], v168, s[22:23] offset:2048
	global_load_dwordx4 v[236:239], v168, s[28:29]
	global_load_dwordx4 v[240:243], v168, s[28:29] offset:2048
	global_load_dwordx4 v[60:63], v168, s[30:31]
	global_load_dwordx4 v[64:67], v168, s[30:31] offset:2048
	global_load_dwordx4 v[68:71], v168, s[34:35]
	global_load_dwordx4 v[72:75], v168, s[34:35] offset:2048
	v_readfirstlane_b32 vcc_lo, v162
	s_ashr_i32 vcc_lo, vcc_lo, 6
	s_mul_i32 vcc_lo, s66, vcc_lo
	s_lshl_b32 vcc_lo, vcc_lo, 4
	v_and_or_b32 v252, v162, 15, s64
	v_add_u32_e32 v252, vcc_lo, v252
	v_lshlrev_b32_e32 v252, 2, v252
	global_load_dword v244, v252, s[26:27]
	global_load_dword v245, v252, s[26:27] offset:64
	global_load_dword v246, v252, s[26:27] offset:128
	global_load_dword v247, v252, s[26:27] offset:192
	v_lshrrev_b32_e32 v5, 4, v162
	v_lshlrev_b32_e32 v3, 11, v3
	s_lshl_b32 s10, s10, 8
	s_and_b32 s10, s10, 0xffffc000
	v_and_b32_e32 v4, 15, v162
	s_add_i32 s67, s10, 0
	s_add_i32 s68, s67, 0x400
	s_mov_b64 s[10:11], -1
	s_mov_b64 s[12:13], 0
	s_cmp_lt_i32 s66, 2
	s_mov_b64 s[14:15], 0
	s_waitcnt vmcnt(19)
	v_lshlrev_b32_e32 v2, 8, v12
	v_and_or_b32 v169, v2, s60, v133
	s_waitcnt vmcnt(18)
	v_lshlrev_b32_e32 v2, 8, v13
	v_and_or_b32 v170, v2, s60, v132
	s_waitcnt vmcnt(17)
	v_lshlrev_b32_e32 v2, 8, v6
	s_waitcnt vmcnt(16)
	v_lshlrev_b32_e32 v6, 8, v7
	v_and_or_b32 v175, v6, s60, v132
	v_and_or_b32 v174, v2, s60, v133
	s_waitcnt vmcnt(15)
	v_lshlrev_b32_e32 v2, 8, v8
	s_waitcnt vmcnt(14)
	v_lshlrev_b32_e32 v6, 8, v9
	v_and_or_b32 v177, v6, s60, v132
	v_lshlrev_b32_e32 v6, 3, v162
	v_and_or_b32 v176, v2, s60, v133
	v_lshlrev_b32_e32 v2, 10, v11
	v_and_b32_e32 v6, 24, v6
	v_add3_u32 v173, s61, v2, v6
	v_bfe_u32 v2, v162, 2, 3
	v_bitop3_b32 v134, v2, v5, 4 bitop3:0x78
	v_bfe_u32 v2, v162, 2, 2
	v_lshlrev_b32_e32 v7, 8, v2
	v_add3_u32 v3, s61, v3, v7
	v_lshrrev_b32_e32 v7, 2, v162
	v_and_or_b32 v2, v7, 4, v2
	v_lshlrev_b32_e32 v2, 5, v2
	v_add3_u32 v171, v3, v6, v2
	v_bfe_u32 v3, v162, 1, 3
	v_bitop3_b32 v3, v5, v3, 3 bitop3:0x6c
	v_lshlrev_b32_e32 v2, 7, v4
	v_lshlrev_b32_e32 v3, 4, v3
	v_add3_u32 v172, s67, v2, v3
	s_cbranch_scc1 .LBB0_881
	s_cmp_gt_i32 s66, 2
	s_cbranch_scc0 .LBB0_875
	s_cmp_eq_u32 s66, 3
	s_mov_b64 s[14:15], -1
	s_cbranch_scc0 .LBB0_876
	s_mov_b32 s10, m0
	s_mov_b32 m0, s67
	s_nop 0
	global_load_lds_dwordx4 v169, s[8:9]
	s_mov_b32 m0, s10
	s_add_i32 s50, s67, 0x800
	s_mov_b32 s10, m0
	s_mov_b32 m0, s68
	s_nop 0
	global_load_lds_dwordx4 v170, s[8:9]
	s_mov_b32 m0, s10
	s_add_i32 s51, s67, 0xc00
	s_mov_b32 s10, m0
	s_mov_b32 m0, s50
	s_nop 0
	global_load_lds_dwordx4 v174, s[8:9]
	s_mov_b32 m0, s10
	s_add_i32 s69, s67, 0x1000
	s_mov_b32 s10, m0
	s_mov_b32 m0, s51
	s_nop 0
	global_load_lds_dwordx4 v175, s[8:9]
	s_mov_b32 m0, s10
	s_add_i32 s70, s67, 0x1400
	s_mov_b32 s10, m0
	s_mov_b32 m0, s69
	s_nop 0
	global_load_lds_dwordx4 v176, s[8:9]
	s_mov_b32 m0, s10
	v_mov_b32_e32 v26, 0
	s_mov_b32 s10, m0
	s_mov_b32 m0, s70
	s_nop 0
	global_load_lds_dwordx4 v177, s[8:9]
	s_mov_b32 m0, s10
	s_waitcnt vmcnt(10)
	v_mov_b32_e32 v106, v60
	v_mov_b32_e32 v107, v61
	v_mov_b32_e32 v108, v62
	v_mov_b32_e32 v109, v63
	v_mov_b32_e32 v102, v64
	v_mov_b32_e32 v103, v65
	v_mov_b32_e32 v104, v66
	v_mov_b32_e32 v105, v67
	v_mov_b32_e32 v110, v68
	v_mov_b32_e32 v111, v69
	v_mov_b32_e32 v112, v70
	v_mov_b32_e32 v113, v71
	v_mov_b32_e32 v98, v72
	v_mov_b32_e32 v99, v73
	v_mov_b32_e32 v100, v74
	v_mov_b32_e32 v101, v75
	v_xor_b32_e32 v139, 64, v172
	v_cvt_pk_bf16_f32 v2, v228, v229
	v_cvt_pk_bf16_f32 v3, v230, v231
	v_lshlrev_b32_e32 v4, 5, v134
	v_add_u32_e32 v135, v173, v4
	v_xor_b32_e32 v5, 32, v4
	ds_write_b64 v135, v[2:3]
	v_cvt_pk_bf16_f32 v2, v232, v233
	v_cvt_pk_bf16_f32 v3, v234, v235
	v_add_u32_e32 v136, v173, v5
	v_xor_b32_e32 v5, 64, v4
	ds_write_b64 v136, v[2:3] offset:256
	v_cvt_pk_bf16_f32 v2, v236, v237
	v_cvt_pk_bf16_f32 v3, v238, v239
	v_add_u32_e32 v137, v173, v5
	v_xor_b32_e32 v4, 0x60, v4
	ds_write_b64 v137, v[2:3] offset:512
	v_cvt_pk_bf16_f32 v2, v240, v241
	v_cvt_pk_bf16_f32 v3, v242, v243
	v_add_u32_e32 v138, v173, v4
	ds_write_b64 v138, v[2:3] offset:768
	global_load_dwordx4 v[122:125], v168, s[36:37]
	global_load_dwordx4 v[118:121], v168, s[36:37] offset:2048
	global_load_dwordx4 v[126:129], v168, s[38:39]
	global_load_dwordx4 v[114:117], v168, s[38:39] offset:2048
	s_waitcnt lgkmcnt(0)
	s_barrier
	v_add_u32_e32 v2, 0x2000, v172
	s_add_i32 s71, s67, 0x2000
	v_xor_b32_e32 v140, 64, v2
	v_xor_b32_e32 v141, 32, v171
	v_xor_b32_e32 v142, 64, v171
	v_xor_b32_e32 v143, 0x60, v171
	v_xor_b32_e32 v144, 0x80, v171
	v_xor_b32_e32 v145, 0xa0, v171
	v_xor_b32_e32 v146, 0xc0, v171
	s_add_i32 s72, s67, 0x2400
	v_xor_b32_e32 v147, 0xe0, v171
	s_add_i32 s73, s67, 0x2800
	s_add_i32 s74, s67, 0x2c00
	s_add_i32 s75, s67, 0x3000
	s_add_i32 s76, s67, 0x3400
	s_mov_b32 s48, 0
	s_mov_b64 s[14:15], 0
	v_mov_b32_e32 v27, v26
	v_mov_b32_e32 v28, v26
	v_mov_b32_e32 v29, v26
	v_mov_b32_e32 v2, v26
	v_mov_b32_e32 v3, v26
	v_mov_b32_e32 v4, v26
	v_mov_b32_e32 v5, v26
	v_mov_b32_e32 v10, v26
	v_mov_b32_e32 v11, v26
	v_mov_b32_e32 v12, v26
	v_mov_b32_e32 v13, v26
	v_mov_b32_e32 v50, v26
	v_mov_b32_e32 v51, v26
	v_mov_b32_e32 v52, v26
	v_mov_b32_e32 v53, v26
	v_mov_b32_e32 v14, v26
	v_mov_b32_e32 v15, v26
	v_mov_b32_e32 v16, v26
	v_mov_b32_e32 v17, v26
	v_mov_b32_e32 v30, v26
	v_mov_b32_e32 v31, v26
	v_mov_b32_e32 v32, v26
	v_mov_b32_e32 v33, v26
	v_mov_b32_e32 v66, v26
	v_mov_b32_e32 v67, v26
	v_mov_b32_e32 v68, v26
	v_mov_b32_e32 v69, v26
	v_mov_b32_e32 v34, v26
	v_mov_b32_e32 v35, v26
	v_mov_b32_e32 v36, v26
	v_mov_b32_e32 v37, v26
	v_mov_b32_e32 v62, v26
	v_mov_b32_e32 v63, v26
	v_mov_b32_e32 v64, v26
	v_mov_b32_e32 v65, v26
	v_mov_b32_e32 v82, v26
	v_mov_b32_e32 v83, v26
	v_mov_b32_e32 v84, v26
	v_mov_b32_e32 v85, v26
	v_mov_b32_e32 v54, v26
	v_mov_b32_e32 v55, v26
	v_mov_b32_e32 v56, v26
	v_mov_b32_e32 v57, v26
	v_mov_b32_e32 v86, v26
	v_mov_b32_e32 v87, v26
	v_mov_b32_e32 v88, v26
	v_mov_b32_e32 v89, v26
	v_mov_b32_e32 v22, v26
	v_mov_b32_e32 v23, v26
	v_mov_b32_e32 v24, v26
	v_mov_b32_e32 v25, v26
	v_mov_b32_e32 v6, v26
	v_mov_b32_e32 v7, v26
	v_mov_b32_e32 v8, v26
	v_mov_b32_e32 v9, v26
	v_mov_b32_e32 v42, v26
	v_mov_b32_e32 v43, v26
	v_mov_b32_e32 v44, v26
	v_mov_b32_e32 v45, v26
	v_mov_b32_e32 v38, v26
	v_mov_b32_e32 v39, v26
	v_mov_b32_e32 v40, v26
	v_mov_b32_e32 v41, v26
	v_mov_b32_e32 v18, v26
	v_mov_b32_e32 v19, v26
	v_mov_b32_e32 v20, v26
	v_mov_b32_e32 v21, v26
	v_mov_b32_e32 v70, v26
	v_mov_b32_e32 v71, v26
	v_mov_b32_e32 v72, v26
	v_mov_b32_e32 v73, v26
	v_mov_b32_e32 v58, v26
	v_mov_b32_e32 v59, v26
	v_mov_b32_e32 v60, v26
	v_mov_b32_e32 v61, v26
	v_mov_b32_e32 v46, v26
	v_mov_b32_e32 v47, v26
	v_mov_b32_e32 v48, v26
	v_mov_b32_e32 v49, v26
	v_mov_b32_e32 v90, v26
	v_mov_b32_e32 v91, v26
	v_mov_b32_e32 v92, v26
	v_mov_b32_e32 v93, v26
	v_mov_b32_e32 v78, v26
	v_mov_b32_e32 v79, v26
	v_mov_b32_e32 v80, v26
	v_mov_b32_e32 v81, v26
	v_mov_b32_e32 v74, v26
	v_mov_b32_e32 v75, v26
	v_mov_b32_e32 v76, v26
	v_mov_b32_e32 v77, v26
	v_mov_b32_e32 v94, v26
	v_mov_b32_e32 v95, v26
	v_mov_b32_e32 v96, v26
	v_mov_b32_e32 v97, v26

.LBB0_877:
	s_mov_b32 s10, m0
	s_mov_b32 m0, s67
	s_nop 0
	global_load_lds_dwordx4 v169, s[8:9]
	s_mov_b32 m0, s10
	s_add_i32 s69, s67, 0x800
	s_mov_b32 s10, m0
	s_mov_b32 m0, s68
	s_nop 0
	global_load_lds_dwordx4 v170, s[8:9]
	s_mov_b32 m0, s10
	s_add_i32 s70, s67, 0xc00
	s_mov_b32 s10, m0
	s_mov_b32 m0, s69
	s_nop 0
	global_load_lds_dwordx4 v174, s[8:9]
	s_mov_b32 m0, s10
	v_xor_b32_e32 v102, 64, v172
	s_mov_b32 s10, m0
	s_mov_b32 m0, s70
	s_nop 0
	global_load_lds_dwordx4 v175, s[8:9]
	s_mov_b32 m0, s10
	s_waitcnt vmcnt(8)
	v_mov_b32_e32 v38, v60
	v_mov_b32_e32 v39, v61
	v_mov_b32_e32 v40, v62
	v_mov_b32_e32 v41, v63
	v_mov_b32_e32 v26, v64
	v_mov_b32_e32 v27, v65
	v_mov_b32_e32 v28, v66
	v_mov_b32_e32 v29, v67
	v_mov_b32_e32 v50, v68
	v_mov_b32_e32 v51, v69
	v_mov_b32_e32 v52, v70
	v_mov_b32_e32 v53, v71
	v_mov_b32_e32 v22, v72
	v_mov_b32_e32 v23, v73
	v_mov_b32_e32 v24, v74
	v_mov_b32_e32 v25, v75
	s_add_i32 s71, s67, 0x2000
	v_cvt_pk_bf16_f32 v2, v228, v229
	v_cvt_pk_bf16_f32 v3, v230, v231
	v_lshlrev_b32_e32 v4, 5, v134
	v_add_u32_e32 v98, v173, v4
	v_xor_b32_e32 v5, 32, v4
	ds_write_b64 v98, v[2:3]
	v_cvt_pk_bf16_f32 v2, v232, v233
	v_cvt_pk_bf16_f32 v3, v234, v235
	v_add_u32_e32 v99, v173, v5
	v_xor_b32_e32 v5, 64, v4
	ds_write_b64 v99, v[2:3] offset:256
	v_cvt_pk_bf16_f32 v2, v236, v237
	v_cvt_pk_bf16_f32 v3, v238, v239
	v_add_u32_e32 v100, v173, v5
	v_xor_b32_e32 v4, 0x60, v4
	ds_write_b64 v100, v[2:3] offset:512
	v_cvt_pk_bf16_f32 v2, v240, v241
	v_cvt_pk_bf16_f32 v3, v242, v243
	v_add_u32_e32 v101, v173, v4
	ds_write_b64 v101, v[2:3] offset:768
	global_load_dwordx4 v[78:81], v168, s[36:37]
	global_load_dwordx4 v[66:69], v168, s[36:37] offset:2048
	global_load_dwordx4 v[82:85], v168, s[38:39]
	global_load_dwordx4 v[58:61], v168, s[38:39] offset:2048
	s_waitcnt lgkmcnt(0)
	s_barrier
	v_add_u32_e32 v2, 0x2000, v172
	v_xor_b32_e32 v103, 64, v2
	v_mov_b32_e32 v2, 0
	v_xor_b32_e32 v104, 32, v171
	v_xor_b32_e32 v105, 64, v171
	v_xor_b32_e32 v106, 0x60, v171
	v_xor_b32_e32 v107, 0x80, v171
	v_xor_b32_e32 v108, 0xa0, v171
	v_xor_b32_e32 v109, 0xc0, v171
	s_add_i32 s72, s67, 0x2400
	v_xor_b32_e32 v110, 0xe0, v171
	s_add_i32 s73, s67, 0x2800
	s_add_i32 s74, s67, 0x2c00
	s_mov_b32 s50, 0
	s_mov_b64 s[46:47], 0
	v_mov_b32_e32 v3, v2
	v_mov_b32_e32 v4, v2
	v_mov_b32_e32 v5, v2
	v_mov_b32_e32 v10, v2
	v_mov_b32_e32 v11, v2
	v_mov_b32_e32 v12, v2
	v_mov_b32_e32 v13, v2
	v_mov_b32_e32 v14, v2
	v_mov_b32_e32 v15, v2
	v_mov_b32_e32 v16, v2
	v_mov_b32_e32 v17, v2
	v_mov_b32_e32 v30, v2
	v_mov_b32_e32 v31, v2
	v_mov_b32_e32 v32, v2
	v_mov_b32_e32 v33, v2
	v_mov_b32_e32 v34, v2
	v_mov_b32_e32 v35, v2
	v_mov_b32_e32 v36, v2
	v_mov_b32_e32 v37, v2
	v_mov_b32_e32 v62, v2
	v_mov_b32_e32 v63, v2
	v_mov_b32_e32 v64, v2
	v_mov_b32_e32 v65, v2
	v_mov_b32_e32 v54, v2
	v_mov_b32_e32 v55, v2
	v_mov_b32_e32 v56, v2
	v_mov_b32_e32 v57, v2
	v_mov_b32_e32 v86, v2
	v_mov_b32_e32 v87, v2
	v_mov_b32_e32 v88, v2
	v_mov_b32_e32 v89, v2
	v_mov_b32_e32 v6, v2
	v_mov_b32_e32 v7, v2
	v_mov_b32_e32 v8, v2
	v_mov_b32_e32 v9, v2
	v_mov_b32_e32 v42, v2
	v_mov_b32_e32 v43, v2
	v_mov_b32_e32 v44, v2
	v_mov_b32_e32 v45, v2
	v_mov_b32_e32 v18, v2
	v_mov_b32_e32 v19, v2
	v_mov_b32_e32 v20, v2
	v_mov_b32_e32 v21, v2
	v_mov_b32_e32 v70, v2
	v_mov_b32_e32 v71, v2
	v_mov_b32_e32 v72, v2
	v_mov_b32_e32 v73, v2
	v_mov_b32_e32 v46, v2
	v_mov_b32_e32 v47, v2
	v_mov_b32_e32 v48, v2
	v_mov_b32_e32 v49, v2
	v_mov_b32_e32 v90, v2
	v_mov_b32_e32 v91, v2
	v_mov_b32_e32 v92, v2
	v_mov_b32_e32 v93, v2
	v_mov_b32_e32 v74, v2
	v_mov_b32_e32 v75, v2
	v_mov_b32_e32 v76, v2
	v_mov_b32_e32 v77, v2
	v_mov_b32_e32 v94, v2
	v_mov_b32_e32 v95, v2
	v_mov_b32_e32 v96, v2
	v_mov_b32_e32 v97, v2

.LBB0_883:
	v_mov_b32_e32 v125, 0
	v_lshlrev_b32_e32 v98, 5, v134
	v_add_u32_e32 v99, 0x2000, v172
	s_andn2_b64 vcc, exec, s[14:15]
	v_xor_b32_e32 v178, 64, v172
	v_xor_b32_e32 v179, 32, v171
	v_xor_b32_e32 v180, 64, v171
	v_xor_b32_e32 v181, 0x60, v171
	v_xor_b32_e32 v182, 0x80, v171
	v_xor_b32_e32 v183, 0xa0, v171
	v_xor_b32_e32 v184, 0xc0, v171
	v_xor_b32_e32 v185, 0xe0, v171
	v_add_u32_e32 v186, v173, v98
	v_xor_b32_e32 v190, 32, v98
	v_xor_b32_e32 v189, 64, v98
	v_xor_b32_e32 v188, 0x60, v98
	v_xor_b32_e32 v187, 64, v99
	v_mov_b32_e32 v124, v125
	v_mov_b32_e32 v123, v125
	v_mov_b32_e32 v122, v125
	v_mov_b32_e32 v117, v125
	v_mov_b32_e32 v116, v125
	v_mov_b32_e32 v115, v125
	v_mov_b32_e32 v114, v125
	v_mov_b32_e32 v109, v125
	v_mov_b32_e32 v108, v125
	v_mov_b32_e32 v107, v125
	v_mov_b32_e32 v106, v125
	v_mov_b32_e32 v105, v125
	v_mov_b32_e32 v104, v125
	v_mov_b32_e32 v103, v125
	v_mov_b32_e32 v102, v125
	v_mov_b32_e32 v129, v125
	v_mov_b32_e32 v128, v125
	v_mov_b32_e32 v127, v125
	v_mov_b32_e32 v126, v125
	v_mov_b32_e32 v121, v125
	v_mov_b32_e32 v120, v125
	v_mov_b32_e32 v119, v125
	v_mov_b32_e32 v118, v125
	v_mov_b32_e32 v113, v125
	v_mov_b32_e32 v112, v125
	v_mov_b32_e32 v111, v125
	v_mov_b32_e32 v110, v125
	v_mov_b32_e32 v101, v125
	v_mov_b32_e32 v100, v125
	v_mov_b32_e32 v99, v125
	v_mov_b32_e32 v98, v125
	s_cbranch_vccnz .LBB0_887
	s_waitcnt vmcnt(13)
	v_lshlrev_b32_e32 v2, 8, v131
	v_and_or_b32 v191, v2, s60, v133
	s_waitcnt vmcnt(12)
	v_lshlrev_b32_e32 v2, 8, v130
	v_and_or_b32 v192, v2, s60, v132
	s_mov_b32 s10, m0
	s_mov_b32 m0, s67
	s_nop 0
	global_load_lds_dwordx4 v169, s[8:9]
	s_mov_b32 m0, s10
	s_add_i32 s48, s67, 0x800
	s_mov_b32 s10, m0
	s_mov_b32 m0, s68
	s_nop 0
	global_load_lds_dwordx4 v170, s[8:9]
	s_mov_b32 m0, s10
	s_add_i32 s49, s67, 0xc00
	s_mov_b32 s10, m0
	s_mov_b32 m0, s48
	s_nop 0
	global_load_lds_dwordx4 v174, s[8:9]
	s_mov_b32 m0, s10
	s_add_i32 s50, s67, 0x1000
	s_mov_b32 s10, m0
	s_mov_b32 m0, s49
	s_nop 0
	global_load_lds_dwordx4 v175, s[8:9]
	s_mov_b32 m0, s10
	s_add_i32 s51, s67, 0x1400
	s_mov_b32 s10, m0
	s_mov_b32 m0, s50
	s_nop 0
	global_load_lds_dwordx4 v176, s[8:9]
	s_mov_b32 m0, s10
	s_add_i32 s69, s67, 0x1800
	s_mov_b32 s10, m0
	s_mov_b32 m0, s51
	s_nop 0
	global_load_lds_dwordx4 v177, s[8:9]
	s_mov_b32 m0, s10
	s_add_i32 s70, s67, 0x1c00
	s_mov_b32 s10, m0
	s_mov_b32 m0, s69
	s_nop 0
	global_load_lds_dwordx4 v191, s[8:9]
	s_mov_b32 m0, s10
	v_add_u32_e32 v193, v173, v190
	s_mov_b32 s10, m0
	s_mov_b32 m0, s70
	s_nop 0
	global_load_lds_dwordx4 v192, s[8:9]
	s_mov_b32 m0, s10
	s_waitcnt vmcnt(12)
	v_mov_b32_e32 v138, v60
	v_mov_b32_e32 v139, v61
	v_mov_b32_e32 v140, v62
	v_mov_b32_e32 v141, v63
	v_mov_b32_e32 v134, v64
	v_mov_b32_e32 v135, v65
	v_mov_b32_e32 v136, v66
	v_mov_b32_e32 v137, v67
	v_mov_b32_e32 v142, v68
	v_mov_b32_e32 v143, v69
	v_mov_b32_e32 v144, v70
	v_mov_b32_e32 v145, v71
	v_mov_b32_e32 v130, v72
	v_mov_b32_e32 v131, v73
	v_mov_b32_e32 v132, v74
	v_mov_b32_e32 v133, v75
	v_add_u32_e32 v194, v173, v189
	v_cvt_pk_bf16_f32 v2, v228, v229
	v_cvt_pk_bf16_f32 v3, v230, v231
	ds_write_b64 v186, v[2:3]
	v_cvt_pk_bf16_f32 v2, v232, v233
	v_cvt_pk_bf16_f32 v3, v234, v235
	ds_write_b64 v193, v[2:3] offset:256
	v_cvt_pk_bf16_f32 v2, v236, v237
	v_cvt_pk_bf16_f32 v3, v238, v239
	ds_write_b64 v194, v[2:3] offset:512
	v_cvt_pk_bf16_f32 v2, v240, v241
	v_cvt_pk_bf16_f32 v3, v242, v243
	v_add_u32_e32 v195, v173, v188
	ds_write_b64 v195, v[2:3] offset:768
	global_load_dwordx4 v[154:157], v168, s[36:37]
	global_load_dwordx4 v[150:153], v168, s[36:37] offset:2048
	global_load_dwordx4 v[158:161], v168, s[38:39]
	global_load_dwordx4 v[146:149], v168, s[38:39] offset:2048
	s_waitcnt lgkmcnt(0)
	s_barrier
	v_mov_b32_e32 v98, 0
	s_add_i32 s71, s67, 0x2000
	s_add_i32 s72, s67, 0x2400
	s_add_i32 s73, s67, 0x2800
	s_add_i32 s74, s67, 0x2c00
	s_add_i32 s75, s67, 0x3000
	s_add_i32 s76, s67, 0x3400
	s_add_i32 s77, s67, 0x3800
	s_add_i32 s78, s67, 0x3c00
	s_mov_b32 s46, 0
	s_mov_b64 s[12:13], 0
	v_mov_b32_e32 v99, v98
	v_mov_b32_e32 v100, v98
	v_mov_b32_e32 v101, v98
	v_mov_b32_e32 v26, v98
	v_mov_b32_e32 v27, v98
	v_mov_b32_e32 v28, v98
	v_mov_b32_e32 v29, v98
	v_mov_b32_e32 v2, v98
	v_mov_b32_e32 v3, v98
	v_mov_b32_e32 v4, v98
	v_mov_b32_e32 v5, v98
	v_mov_b32_e32 v10, v98
	v_mov_b32_e32 v11, v98
	v_mov_b32_e32 v12, v98
	v_mov_b32_e32 v13, v98
	v_mov_b32_e32 v110, v98
	v_mov_b32_e32 v111, v98
	v_mov_b32_e32 v112, v98
	v_mov_b32_e32 v113, v98
	v_mov_b32_e32 v50, v98
	v_mov_b32_e32 v51, v98
	v_mov_b32_e32 v52, v98
	v_mov_b32_e32 v53, v98
	v_mov_b32_e32 v14, v98
	v_mov_b32_e32 v15, v98
	v_mov_b32_e32 v16, v98
	v_mov_b32_e32 v17, v98
	v_mov_b32_e32 v30, v98
	v_mov_b32_e32 v31, v98
	v_mov_b32_e32 v32, v98
	v_mov_b32_e32 v33, v98
	v_mov_b32_e32 v118, v98
	v_mov_b32_e32 v119, v98
	v_mov_b32_e32 v120, v98
	v_mov_b32_e32 v121, v98
	v_mov_b32_e32 v66, v98
	v_mov_b32_e32 v67, v98
	v_mov_b32_e32 v68, v98
	v_mov_b32_e32 v69, v98
	v_mov_b32_e32 v34, v98
	v_mov_b32_e32 v35, v98
	v_mov_b32_e32 v36, v98
	v_mov_b32_e32 v37, v98
	v_mov_b32_e32 v62, v98
	v_mov_b32_e32 v63, v98
	v_mov_b32_e32 v64, v98
	v_mov_b32_e32 v65, v98
	v_mov_b32_e32 v126, v98
	v_mov_b32_e32 v127, v98
	v_mov_b32_e32 v128, v98
	v_mov_b32_e32 v129, v98
	v_mov_b32_e32 v82, v98
	v_mov_b32_e32 v83, v98
	v_mov_b32_e32 v84, v98
	v_mov_b32_e32 v85, v98
	v_mov_b32_e32 v54, v98
	v_mov_b32_e32 v55, v98
	v_mov_b32_e32 v56, v98
	v_mov_b32_e32 v57, v98
	v_mov_b32_e32 v86, v98
	v_mov_b32_e32 v87, v98
	v_mov_b32_e32 v88, v98
	v_mov_b32_e32 v89, v98
	v_mov_b32_e32 v102, v98
	v_mov_b32_e32 v103, v98
	v_mov_b32_e32 v104, v98
	v_mov_b32_e32 v105, v98
	v_mov_b32_e32 v22, v98
	v_mov_b32_e32 v23, v98
	v_mov_b32_e32 v24, v98
	v_mov_b32_e32 v25, v98
	v_mov_b32_e32 v6, v98
	v_mov_b32_e32 v7, v98
	v_mov_b32_e32 v8, v98
	v_mov_b32_e32 v9, v98
	v_mov_b32_e32 v42, v98
	v_mov_b32_e32 v43, v98
	v_mov_b32_e32 v44, v98
	v_mov_b32_e32 v45, v98
	v_mov_b32_e32 v106, v98
	v_mov_b32_e32 v107, v98
	v_mov_b32_e32 v108, v98
	v_mov_b32_e32 v109, v98
	v_mov_b32_e32 v38, v98
	v_mov_b32_e32 v39, v98
	v_mov_b32_e32 v40, v98
	v_mov_b32_e32 v41, v98
	v_mov_b32_e32 v18, v98
	v_mov_b32_e32 v19, v98
	v_mov_b32_e32 v20, v98
	v_mov_b32_e32 v21, v98
	v_mov_b32_e32 v70, v98
	v_mov_b32_e32 v71, v98
	v_mov_b32_e32 v72, v98
	v_mov_b32_e32 v73, v98
	v_mov_b32_e32 v114, v98
	v_mov_b32_e32 v115, v98
	v_mov_b32_e32 v116, v98
	v_mov_b32_e32 v117, v98
	v_mov_b32_e32 v58, v98
	v_mov_b32_e32 v59, v98
	v_mov_b32_e32 v60, v98
	v_mov_b32_e32 v61, v98
	v_mov_b32_e32 v46, v98
	v_mov_b32_e32 v47, v98
	v_mov_b32_e32 v48, v98
	v_mov_b32_e32 v49, v98
	v_mov_b32_e32 v90, v98
	v_mov_b32_e32 v91, v98
	v_mov_b32_e32 v92, v98
	v_mov_b32_e32 v93, v98
	v_mov_b32_e32 v122, v98
	v_mov_b32_e32 v123, v98
	v_mov_b32_e32 v124, v98
	v_mov_b32_e32 v125, v98
	v_mov_b32_e32 v78, v98
	v_mov_b32_e32 v79, v98
	v_mov_b32_e32 v80, v98
	v_mov_b32_e32 v81, v98
	v_mov_b32_e32 v74, v98
	v_mov_b32_e32 v75, v98
	v_mov_b32_e32 v76, v98
	v_mov_b32_e32 v77, v98
	v_mov_b32_e32 v94, v98
	v_mov_b32_e32 v95, v98
	v_mov_b32_e32 v96, v98
	v_mov_b32_e32 v97, v98

.LBB0_887:
	s_and_b64 vcc, exec, s[12:13]
	s_cbranch_vccz .LBB0_891
	s_mov_b32 s10, m0
	s_mov_b32 m0, s67
	s_nop 0
	global_load_lds_dwordx4 v169, s[8:9]
	s_mov_b32 m0, s10
	v_add_u32_e32 v47, v173, v189
	s_mov_b32 s10, m0
	s_mov_b32 m0, s68
	s_nop 0
	global_load_lds_dwordx4 v170, s[8:9]
	s_mov_b32 m0, s10
	s_waitcnt vmcnt(6)
	v_mov_b32_e32 v18, v60
	v_mov_b32_e32 v19, v61
	v_mov_b32_e32 v20, v62
	v_mov_b32_e32 v21, v63
	v_mov_b32_e32 v6, v64
	v_mov_b32_e32 v7, v65
	v_mov_b32_e32 v8, v66
	v_mov_b32_e32 v9, v67
	v_mov_b32_e32 v14, v68
	v_mov_b32_e32 v15, v69
	v_mov_b32_e32 v16, v70
	v_mov_b32_e32 v17, v71
	v_mov_b32_e32 v2, v72
	v_mov_b32_e32 v3, v73
	v_mov_b32_e32 v4, v74
	v_mov_b32_e32 v5, v75
	v_add_u32_e32 v46, v173, v190
	v_cvt_pk_bf16_f32 v10, v228, v229
	v_cvt_pk_bf16_f32 v11, v230, v231
	ds_write_b64 v186, v[10:11]
	v_cvt_pk_bf16_f32 v10, v236, v237
	v_cvt_pk_bf16_f32 v11, v238, v239
	v_cvt_pk_bf16_f32 v12, v232, v233
	v_cvt_pk_bf16_f32 v13, v234, v235
	ds_write_b64 v47, v[10:11] offset:512
	v_cvt_pk_bf16_f32 v10, v240, v241
	v_cvt_pk_bf16_f32 v11, v242, v243
	v_add_u32_e32 v48, v173, v188
	ds_write_b64 v46, v[12:13] offset:256
	ds_write_b64 v48, v[10:11] offset:768
	global_load_dwordx4 v[38:41], v168, s[36:37]
	global_load_dwordx4 v[26:29], v168, s[36:37] offset:2048
	global_load_dwordx4 v[34:37], v168, s[38:39]
	global_load_dwordx4 v[22:25], v168, s[38:39] offset:2048
	s_waitcnt lgkmcnt(0)
	s_barrier
	v_mov_b32_e32 v10, 0
	s_add_i32 s46, s67, 0x2000
	s_add_i32 s47, s67, 0x2400
	s_mov_b32 s48, 0
	s_mov_b64 s[12:13], 0
	v_mov_b32_e32 v11, v10
	v_mov_b32_e32 v12, v10
	v_mov_b32_e32 v13, v10
	v_mov_b32_e32 v30, v10
	v_mov_b32_e32 v31, v10
	v_mov_b32_e32 v32, v10
	v_mov_b32_e32 v33, v10
	v_mov_b32_e32 v62, v10
	v_mov_b32_e32 v63, v10
	v_mov_b32_e32 v64, v10
	v_mov_b32_e32 v65, v10
	v_mov_b32_e32 v86, v10
	v_mov_b32_e32 v87, v10
	v_mov_b32_e32 v88, v10
	v_mov_b32_e32 v89, v10
	v_mov_b32_e32 v42, v10
	v_mov_b32_e32 v43, v10
	v_mov_b32_e32 v44, v10
	v_mov_b32_e32 v45, v10
	v_mov_b32_e32 v70, v10
	v_mov_b32_e32 v71, v10
	v_mov_b32_e32 v72, v10
	v_mov_b32_e32 v73, v10
	v_mov_b32_e32 v90, v10
	v_mov_b32_e32 v91, v10
	v_mov_b32_e32 v92, v10
	v_mov_b32_e32 v93, v10
	v_mov_b32_e32 v94, v10
	v_mov_b32_e32 v95, v10
	v_mov_b32_e32 v96, v10
	v_mov_b32_e32 v97, v10

.LBB0_891:
	s_nop 0
	v_readfirstlane_b32 s10, v162
	s_ashr_i32 s10, s10, 6
	s_mul_i32 s66, s66, s10
	s_waitcnt vmcnt(1)
	v_and_or_b32 v131, v162, 15, s64
	s_waitcnt vmcnt(0)
	v_lshrrev_b32_e32 v130, 2, v162
	s_lshl_b32 s48, s66, 4
	v_and_b32_e32 v130, 12, v130
	v_add_u32_e32 v132, s48, v131
	v_cmp_gt_i32_e32 vcc, s65, v132
	v_lshlrev_b32_e32 v162, 1, v130
	s_and_saveexec_b64 s[46:47], vcc
	s_cbranch_execz .LBB0_893
	v_ashrrev_i32_e32 v133, 31, v132
	v_lshl_add_u64 v[134:135], v[132:133], 2, s[26:27]
	v_mul_f32_e32 v134, 0xbfb8aa3b, v94
	v_mul_f32_e32 v135, 0xbfb8aa3b, v95
	v_exp_f32_e32 v134, v134
	v_exp_f32_e32 v135, v135
	v_mul_f32_e32 v136, 0xbfb8aa3b, v96
	v_mul_f32_e32 v137, 0xbfb8aa3b, v97
	v_exp_f32_e32 v136, v136
	v_exp_f32_e32 v137, v137
	v_pk_add_f32 v[134:135], v[134:135], 1.0 op_sel_hi:[1,0]
	v_mul_f32_e32 v138, 0xbfb8aa3b, v90
	v_pk_add_f32 v[136:137], v[136:137], 1.0 op_sel_hi:[1,0]
	v_mul_f32_e32 v139, 0xbfb8aa3b, v91
	v_exp_f32_e32 v138, v138
	v_exp_f32_e32 v139, v139
	v_rcp_f32_e32 v140, v135
	s_nop 0
	v_mul_f32_e32 v95, v95, v140
	v_rcp_f32_e32 v135, v134
	s_nop 0
	v_mul_f32_e32 v94, v94, v135
	v_pk_mul_f32 v[86:87], v[86:87], v[94:95]
	v_pk_add_f32 v[138:139], v[138:139], 1.0 op_sel_hi:[1,0]
	v_rcp_f32_e32 v134, v137
	s_nop 0
	v_mul_f32_e32 v95, v97, v134
	v_rcp_f32_e32 v94, v136
	s_nop 0
	v_mul_f32_e32 v94, v96, v94
	v_add_u32_e32 v132, s63, v132
	v_pk_mul_f32 v[88:89], v[88:89], v[94:95]
	v_ashrrev_i32_e32 v133, 31, v132
	v_lshlrev_b64 v[132:133], 9, v[132:133]
	v_lshl_add_u64 v[132:133], s[20:21], 0, v[132:133]
	v_mov_b32_e32 v130, v244
	v_pk_mul_f32 v[86:87], v[86:87], v[130:131] op_sel_hi:[1,0]
	v_pk_mul_f32 v[88:89], v[88:89], v[130:131] op_sel_hi:[1,0]
	v_lshl_add_u64 v[132:133], v[132:133], 0, v[162:163]
	v_cvt_pk_bf16_f32 v86, v86, v87
	v_cvt_pk_bf16_f32 v87, v88, v89
	global_store_dwordx2 v[132:133], v[86:87], off
	v_rcp_f32_e32 v86, v139
	s_nop 0
	v_mul_f32_e32 v87, v91, v86
	v_mul_f32_e32 v88, 0xbfb8aa3b, v92
	v_mul_f32_e32 v89, 0xbfb8aa3b, v93
	v_exp_f32_e32 v88, v88
	v_exp_f32_e32 v89, v89
	v_rcp_f32_e32 v86, v138
	s_nop 0
	v_mul_f32_e32 v86, v90, v86
	v_pk_mul_f32 v[62:63], v[62:63], v[86:87]
	v_pk_add_f32 v[88:89], v[88:89], 1.0 op_sel_hi:[1,0]
	v_pk_mul_f32 v[62:63], v[62:63], v[130:131] op_sel_hi:[1,0]
	v_cvt_pk_bf16_f32 v62, v62, v63
	v_rcp_f32_e32 v63, v89
	s_nop 0
	v_mul_f32_e32 v87, v93, v63
	v_mul_f32_e32 v89, 0xbfb8aa3b, v70
	v_exp_f32_e32 v90, v89
	v_mul_f32_e32 v89, 0xbfb8aa3b, v71
	v_exp_f32_e32 v91, v89
	v_rcp_f32_e32 v63, v88
	s_nop 0
	v_mul_f32_e32 v86, v92, v63
	v_pk_mul_f32 v[64:65], v[64:65], v[86:87]
	v_pk_add_f32 v[86:87], v[90:91], 1.0 op_sel_hi:[1,0]
	v_pk_mul_f32 v[64:65], v[64:65], v[130:131] op_sel_hi:[1,0]
	v_cvt_pk_bf16_f32 v63, v64, v65
	global_store_dwordx2 v[132:133], v[62:63], off offset:32
	v_rcp_f32_e32 v62, v87
	s_nop 0
	v_mul_f32_e32 v63, v71, v62
	v_mul_f32_e32 v64, 0xbfb8aa3b, v72
	v_mul_f32_e32 v65, 0xbfb8aa3b, v73
	v_exp_f32_e32 v64, v64
	v_exp_f32_e32 v65, v65
	v_rcp_f32_e32 v62, v86
	s_nop 0
	v_mul_f32_e32 v62, v70, v62
	v_pk_mul_f32 v[30:31], v[30:31], v[62:63]
	v_pk_add_f32 v[64:65], v[64:65], 1.0 op_sel_hi:[1,0]
	v_pk_mul_f32 v[30:31], v[30:31], v[130:131] op_sel_hi:[1,0]
	v_cvt_pk_bf16_f32 v30, v30, v31
	v_rcp_f32_e32 v31, v65
	s_nop 0
	v_mul_f32_e32 v63, v73, v31
	v_mul_f32_e32 v65, 0xbfb8aa3b, v42
	v_exp_f32_e32 v70, v65
	v_mul_f32_e32 v65, 0xbfb8aa3b, v43
	v_exp_f32_e32 v71, v65
	v_rcp_f32_e32 v31, v64
	s_nop 0
	v_mul_f32_e32 v62, v72, v31
	v_pk_mul_f32 v[32:33], v[32:33], v[62:63]
	v_pk_add_f32 v[62:63], v[70:71], 1.0 op_sel_hi:[1,0]
	v_pk_mul_f32 v[32:33], v[32:33], v[130:131] op_sel_hi:[1,0]
	v_cvt_pk_bf16_f32 v31, v32, v33
	global_store_dwordx2 v[132:133], v[30:31], off offset:64
	v_rcp_f32_e32 v30, v63
	s_nop 0
	v_mul_f32_e32 v31, v43, v30
	v_mul_f32_e32 v32, 0xbfb8aa3b, v44
	v_mul_f32_e32 v33, 0xbfb8aa3b, v45
	v_exp_f32_e32 v32, v32
	v_exp_f32_e32 v33, v33
	v_rcp_f32_e32 v30, v62
	s_nop 0
	v_mul_f32_e32 v30, v42, v30
	v_pk_mul_f32 v[10:11], v[10:11], v[30:31]
	v_pk_add_f32 v[32:33], v[32:33], 1.0 op_sel_hi:[1,0]
	v_pk_mul_f32 v[10:11], v[10:11], v[130:131] op_sel_hi:[1,0]
	v_cvt_pk_bf16_f32 v10, v10, v11
	v_rcp_f32_e32 v11, v33
	s_nop 0
	v_mul_f32_e32 v31, v45, v11
	v_rcp_f32_e32 v11, v32
	s_nop 0
	v_mul_f32_e32 v30, v44, v11
	v_pk_mul_f32 v[12:13], v[12:13], v[30:31]
	s_nop 0
	v_pk_mul_f32 v[12:13], v[12:13], v[130:131] op_sel_hi:[1,0]
	s_nop 0
	v_cvt_pk_bf16_f32 v11, v12, v13
	global_store_dwordx2 v[132:133], v[10:11], off offset:96
.LBB0_893:
	s_or_b64 exec, exec, s[46:47]
	v_or_b32_e32 v10, 16, v131
	v_add_u32_e32 v12, s48, v10
	v_cmp_gt_i32_e32 vcc, s65, v12
	s_and_b64 s[10:11], s[44:45], vcc
	s_and_saveexec_b64 s[44:45], s[10:11]
	s_cbranch_execz .LBB0_895
	v_ashrrev_i32_e32 v13, 31, v12
	v_lshl_add_u64 v[10:11], v[12:13], 2, s[26:27]
	v_mul_f32_e32 v11, 0xbfb8aa3b, v74
	v_mul_f32_e32 v31, 0xbfb8aa3b, v75
	v_exp_f32_e32 v30, v11
	v_exp_f32_e32 v31, v31
	v_mul_f32_e32 v32, 0xbfb8aa3b, v76
	v_mul_f32_e32 v33, 0xbfb8aa3b, v77
	v_exp_f32_e32 v32, v32
	v_exp_f32_e32 v33, v33
	v_pk_add_f32 v[30:31], v[30:31], 1.0 op_sel_hi:[1,0]
	v_mul_f32_e32 v42, 0xbfb8aa3b, v46
	v_pk_add_f32 v[32:33], v[32:33], 1.0 op_sel_hi:[1,0]
	v_mul_f32_e32 v43, 0xbfb8aa3b, v47
	v_exp_f32_e32 v42, v42
	v_exp_f32_e32 v43, v43
	v_rcp_f32_e32 v11, v31
	s_nop 0
	v_mul_f32_e32 v31, v75, v11
	v_rcp_f32_e32 v11, v30
	s_nop 0
	v_mul_f32_e32 v30, v74, v11
	v_pk_add_f32 v[42:43], v[42:43], 1.0 op_sel_hi:[1,0]
	v_pk_mul_f32 v[30:31], v[54:55], v[30:31]
	v_rcp_f32_e32 v11, v33
	s_nop 0
	v_mul_f32_e32 v33, v77, v11
	v_add_u32_e32 v12, s63, v12
	v_rcp_f32_e32 v11, v32
	s_nop 0
	v_mul_f32_e32 v32, v76, v11
	v_ashrrev_i32_e32 v13, 31, v12
	v_lshlrev_b64 v[12:13], 9, v[12:13]
	v_pk_mul_f32 v[32:33], v[56:57], v[32:33]
	v_lshl_add_u64 v[12:13], s[20:21], 0, v[12:13]
	v_lshl_add_u64 v[12:13], v[12:13], 0, v[162:163]
	v_mov_b32_e32 v10, v245
	v_pk_mul_f32 v[30:31], v[30:31], v[10:11] op_sel_hi:[1,0]
	v_pk_mul_f32 v[32:33], v[32:33], v[10:11] op_sel_hi:[1,0]
	v_cvt_pk_bf16_f32 v30, v30, v31
	v_cvt_pk_bf16_f32 v31, v32, v33
	global_store_dwordx2 v[12:13], v[30:31], off
	v_rcp_f32_e32 v11, v43
	s_nop 0
	v_mul_f32_e32 v31, v47, v11
	v_mul_f32_e32 v30, 0xbfb8aa3b, v48
	v_exp_f32_e32 v32, v30
	v_mul_f32_e32 v30, 0xbfb8aa3b, v49
	v_exp_f32_e32 v33, v30
	v_rcp_f32_e32 v11, v42
	s_nop 0
	v_mul_f32_e32 v30, v46, v11
	v_pk_mul_f32 v[30:31], v[34:35], v[30:31]
	v_pk_add_f32 v[32:33], v[32:33], 1.0 op_sel_hi:[1,0]
	s_nop 0
	v_pk_mul_f32 v[30:31], v[30:31], v[10:11] op_sel_hi:[1,0]
	s_nop 0
	v_cvt_pk_bf16_f32 v30, v30, v31
	v_rcp_f32_e32 v11, v33
	s_nop 0
	v_mul_f32_e32 v33, v49, v11
	v_mul_f32_e32 v31, 0xbfb8aa3b, v18
	v_exp_f32_e32 v34, v31
	v_mul_f32_e32 v31, 0xbfb8aa3b, v19
	v_exp_f32_e32 v35, v31
	v_rcp_f32_e32 v11, v32
	s_nop 0
	v_mul_f32_e32 v32, v48, v11
	v_pk_mul_f32 v[32:33], v[36:37], v[32:33]
	v_pk_add_f32 v[34:35], v[34:35], 1.0 op_sel_hi:[1,0]
	s_nop 0
	v_pk_mul_f32 v[32:33], v[32:33], v[10:11] op_sel_hi:[1,0]
	s_nop 0
	v_cvt_pk_bf16_f32 v31, v32, v33
	global_store_dwordx2 v[12:13], v[30:31], off offset:32
	v_rcp_f32_e32 v11, v35
	s_nop 0
	v_mul_f32_e32 v19, v19, v11
	v_mul_f32_e32 v30, 0xbfb8aa3b, v20
	v_mul_f32_e32 v31, 0xbfb8aa3b, v21
	v_exp_f32_e32 v30, v30
	v_exp_f32_e32 v31, v31
	v_rcp_f32_e32 v11, v34
	s_nop 0
	v_mul_f32_e32 v18, v18, v11
	v_pk_mul_f32 v[14:15], v[14:15], v[18:19]
	v_pk_add_f32 v[30:31], v[30:31], 1.0 op_sel_hi:[1,0]
	s_nop 0
	v_pk_mul_f32 v[14:15], v[14:15], v[10:11] op_sel_hi:[1,0]
	s_nop 0
	v_cvt_pk_bf16_f32 v14, v14, v15
	v_rcp_f32_e32 v11, v31
	s_nop 0
	v_mul_f32_e32 v19, v21, v11
	v_mul_f32_e32 v15, 0xbfb8aa3b, v6
	v_exp_f32_e32 v32, v15
	v_mul_f32_e32 v15, 0xbfb8aa3b, v7
	v_exp_f32_e32 v33, v15
	v_rcp_f32_e32 v11, v30
	s_nop 0
	v_mul_f32_e32 v18, v20, v11
	v_pk_mul_f32 v[16:17], v[16:17], v[18:19]
	v_pk_add_f32 v[18:19], v[32:33], 1.0 op_sel_hi:[1,0]
	s_nop 0
	v_pk_mul_f32 v[16:17], v[16:17], v[10:11] op_sel_hi:[1,0]
	s_nop 0
	v_cvt_pk_bf16_f32 v15, v16, v17
	global_store_dwordx2 v[12:13], v[14:15], off offset:64
	v_rcp_f32_e32 v11, v19
	s_nop 0
	v_mul_f32_e32 v7, v7, v11
	v_mul_f32_e32 v14, 0xbfb8aa3b, v8
	v_mul_f32_e32 v15, 0xbfb8aa3b, v9
	v_exp_f32_e32 v14, v14
	v_exp_f32_e32 v15, v15
	v_rcp_f32_e32 v11, v18
	s_nop 0
	v_mul_f32_e32 v6, v6, v11
	v_pk_mul_f32 v[2:3], v[2:3], v[6:7]
	v_pk_add_f32 v[14:15], v[14:15], 1.0 op_sel_hi:[1,0]
	s_nop 0
	v_pk_mul_f32 v[2:3], v[2:3], v[10:11] op_sel_hi:[1,0]
	s_nop 0
	v_cvt_pk_bf16_f32 v2, v2, v3
	v_rcp_f32_e32 v3, v15
	s_nop 0
	v_mul_f32_e32 v7, v9, v3
	v_rcp_f32_e32 v3, v14
	s_nop 0
	v_mul_f32_e32 v6, v8, v3
	v_pk_mul_f32 v[4:5], v[4:5], v[6:7]
	s_nop 0
	v_pk_mul_f32 v[4:5], v[4:5], v[10:11] op_sel_hi:[1,0]
	s_nop 0
	v_cvt_pk_bf16_f32 v3, v4, v5
	global_store_dwordx2 v[12:13], v[2:3], off offset:96
.LBB0_895:
	s_or_b64 exec, exec, s[44:45]
	v_or_b32_e32 v2, 32, v131
	v_add_u32_e32 v4, s48, v2
	v_cmp_gt_i32_e32 vcc, s65, v4
	s_and_b64 s[10:11], s[42:43], vcc
	s_and_saveexec_b64 s[42:43], s[10:11]
	s_cbranch_execz .LBB0_897
	v_ashrrev_i32_e32 v5, 31, v4
	v_lshl_add_u64 v[2:3], v[4:5], 2, s[26:27]
	v_mul_f32_e32 v3, 0xbfb8aa3b, v78
	v_mul_f32_e32 v7, 0xbfb8aa3b, v79
	v_exp_f32_e32 v6, v3
	v_exp_f32_e32 v7, v7
	v_mul_f32_e32 v8, 0xbfb8aa3b, v80
	v_mul_f32_e32 v9, 0xbfb8aa3b, v81
	v_exp_f32_e32 v8, v8
	v_exp_f32_e32 v9, v9
	v_pk_add_f32 v[6:7], v[6:7], 1.0 op_sel_hi:[1,0]
	v_mul_f32_e32 v10, 0xbfb8aa3b, v58
	v_pk_add_f32 v[8:9], v[8:9], 1.0 op_sel_hi:[1,0]
	v_mul_f32_e32 v11, 0xbfb8aa3b, v59
	v_exp_f32_e32 v10, v10
	v_exp_f32_e32 v11, v11
	v_rcp_f32_e32 v3, v7
	s_nop 0
	v_mul_f32_e32 v7, v79, v3
	v_rcp_f32_e32 v3, v6
	s_nop 0
	v_mul_f32_e32 v6, v78, v3
	v_pk_add_f32 v[10:11], v[10:11], 1.0 op_sel_hi:[1,0]
	v_pk_mul_f32 v[6:7], v[82:83], v[6:7]
	v_rcp_f32_e32 v3, v9
	s_nop 0
	v_mul_f32_e32 v9, v81, v3
	v_add_u32_e32 v4, s63, v4
	v_rcp_f32_e32 v3, v8
	s_nop 0
	v_mul_f32_e32 v8, v80, v3
	v_ashrrev_i32_e32 v5, 31, v4
	v_lshlrev_b64 v[4:5], 9, v[4:5]
	v_pk_mul_f32 v[8:9], v[84:85], v[8:9]
	v_lshl_add_u64 v[4:5], s[20:21], 0, v[4:5]
	v_lshl_add_u64 v[4:5], v[4:5], 0, v[162:163]
	v_mov_b32_e32 v2, v246
	v_pk_mul_f32 v[6:7], v[6:7], v[2:3] op_sel_hi:[1,0]
	v_pk_mul_f32 v[8:9], v[8:9], v[2:3] op_sel_hi:[1,0]
	v_cvt_pk_bf16_f32 v6, v6, v7
	v_cvt_pk_bf16_f32 v7, v8, v9
	global_store_dwordx2 v[4:5], v[6:7], off
	v_rcp_f32_e32 v3, v11
	s_nop 0
	v_mul_f32_e32 v7, v59, v3
	v_mul_f32_e32 v6, 0xbfb8aa3b, v60
	v_exp_f32_e32 v8, v6
	v_mul_f32_e32 v6, 0xbfb8aa3b, v61
	v_exp_f32_e32 v9, v6
	v_rcp_f32_e32 v3, v10
	s_nop 0
	v_mul_f32_e32 v6, v58, v3
	v_pk_mul_f32 v[6:7], v[66:67], v[6:7]
	v_pk_add_f32 v[8:9], v[8:9], 1.0 op_sel_hi:[1,0]
	s_nop 0
	v_pk_mul_f32 v[6:7], v[6:7], v[2:3] op_sel_hi:[1,0]
	s_nop 0
	v_cvt_pk_bf16_f32 v6, v6, v7
	v_rcp_f32_e32 v3, v9
	s_nop 0
	v_mul_f32_e32 v9, v61, v3
	v_mul_f32_e32 v7, 0xbfb8aa3b, v38
	v_exp_f32_e32 v10, v7
	v_mul_f32_e32 v7, 0xbfb8aa3b, v39
	v_exp_f32_e32 v11, v7
	v_rcp_f32_e32 v3, v8
	s_nop 0
	v_mul_f32_e32 v8, v60, v3
	v_pk_mul_f32 v[8:9], v[68:69], v[8:9]
	v_pk_add_f32 v[10:11], v[10:11], 1.0 op_sel_hi:[1,0]
	s_nop 0
	v_pk_mul_f32 v[8:9], v[8:9], v[2:3] op_sel_hi:[1,0]
	s_nop 0
	v_cvt_pk_bf16_f32 v7, v8, v9
	global_store_dwordx2 v[4:5], v[6:7], off offset:32
	v_rcp_f32_e32 v3, v11
	s_nop 0
	v_mul_f32_e32 v7, v39, v3
	v_mul_f32_e32 v6, 0xbfb8aa3b, v40
	v_exp_f32_e32 v8, v6
	v_mul_f32_e32 v6, 0xbfb8aa3b, v41
	v_exp_f32_e32 v9, v6
	v_rcp_f32_e32 v3, v10
	s_nop 0
	v_mul_f32_e32 v6, v38, v3
	v_pk_mul_f32 v[6:7], v[50:51], v[6:7]
	v_pk_add_f32 v[8:9], v[8:9], 1.0 op_sel_hi:[1,0]
	s_nop 0
	v_pk_mul_f32 v[6:7], v[6:7], v[2:3] op_sel_hi:[1,0]
	s_nop 0
	v_cvt_pk_bf16_f32 v6, v6, v7
	v_rcp_f32_e32 v3, v9
	s_nop 0
	v_mul_f32_e32 v9, v41, v3
	v_mul_f32_e32 v7, 0xbfb8aa3b, v22
	v_exp_f32_e32 v10, v7
	v_mul_f32_e32 v7, 0xbfb8aa3b, v23
	v_exp_f32_e32 v11, v7
	v_rcp_f32_e32 v3, v8
	s_nop 0
	v_mul_f32_e32 v8, v40, v3
	v_pk_mul_f32 v[8:9], v[52:53], v[8:9]
	v_pk_add_f32 v[10:11], v[10:11], 1.0 op_sel_hi:[1,0]
	s_nop 0
	v_pk_mul_f32 v[8:9], v[8:9], v[2:3] op_sel_hi:[1,0]
	s_nop 0
	v_cvt_pk_bf16_f32 v7, v8, v9
	global_store_dwordx2 v[4:5], v[6:7], off offset:64
	v_rcp_f32_e32 v3, v11
	s_nop 0
	v_mul_f32_e32 v7, v23, v3
	v_mul_f32_e32 v6, 0xbfb8aa3b, v24
	v_exp_f32_e32 v8, v6
	v_mul_f32_e32 v6, 0xbfb8aa3b, v25
	v_exp_f32_e32 v9, v6
	v_rcp_f32_e32 v3, v10
	s_nop 0
	v_mul_f32_e32 v6, v22, v3
	v_pk_mul_f32 v[6:7], v[26:27], v[6:7]
	v_pk_add_f32 v[8:9], v[8:9], 1.0 op_sel_hi:[1,0]
	s_nop 0
	v_pk_mul_f32 v[6:7], v[6:7], v[2:3] op_sel_hi:[1,0]
	s_nop 0
	v_cvt_pk_bf16_f32 v6, v6, v7
	v_rcp_f32_e32 v3, v9
	s_nop 0
	v_mul_f32_e32 v9, v25, v3
	v_rcp_f32_e32 v3, v8
	s_nop 0
	v_mul_f32_e32 v8, v24, v3
	v_pk_mul_f32 v[8:9], v[28:29], v[8:9]
	s_nop 0
	v_pk_mul_f32 v[2:3], v[8:9], v[2:3] op_sel_hi:[1,0]
	s_nop 0
	v_cvt_pk_bf16_f32 v7, v2, v3
	global_store_dwordx2 v[4:5], v[6:7], off offset:96
.LBB0_897:
	s_or_b64 exec, exec, s[42:43]
	v_or_b32_e32 v2, 48, v131
	v_add_u32_e32 v4, s48, v2
	v_cmp_gt_i32_e32 vcc, s65, v4
	s_and_b64 s[10:11], s[40:41], vcc
	s_and_saveexec_b64 s[40:41], s[10:11]
	s_cbranch_execz .LBB0_868
	v_ashrrev_i32_e32 v5, 31, v4
	v_lshl_add_u64 v[2:3], v[4:5], 2, s[26:27]
	v_mul_f32_e32 v3, 0xbfb8aa3b, v122
	v_mul_f32_e32 v7, 0xbfb8aa3b, v123
	v_exp_f32_e32 v6, v3
	v_exp_f32_e32 v7, v7
	v_mul_f32_e32 v8, 0xbfb8aa3b, v124
	v_mul_f32_e32 v9, 0xbfb8aa3b, v125
	v_exp_f32_e32 v8, v8
	v_exp_f32_e32 v9, v9
	v_pk_add_f32 v[6:7], v[6:7], 1.0 op_sel_hi:[1,0]
	v_mul_f32_e32 v10, 0xbfb8aa3b, v114
	v_pk_add_f32 v[8:9], v[8:9], 1.0 op_sel_hi:[1,0]
	v_mul_f32_e32 v11, 0xbfb8aa3b, v115
	v_exp_f32_e32 v10, v10
	v_exp_f32_e32 v11, v11
	v_rcp_f32_e32 v3, v7
	s_nop 0
	v_mul_f32_e32 v7, v123, v3
	v_rcp_f32_e32 v3, v6
	s_nop 0
	v_mul_f32_e32 v6, v122, v3
	v_pk_add_f32 v[10:11], v[10:11], 1.0 op_sel_hi:[1,0]
	v_pk_mul_f32 v[6:7], v[126:127], v[6:7]
	v_rcp_f32_e32 v3, v9
	s_nop 0
	v_mul_f32_e32 v9, v125, v3
	v_add_u32_e32 v4, s63, v4
	v_rcp_f32_e32 v3, v8
	s_nop 0
	v_mul_f32_e32 v8, v124, v3
	v_ashrrev_i32_e32 v5, 31, v4
	v_lshlrev_b64 v[4:5], 9, v[4:5]
	v_pk_mul_f32 v[8:9], v[128:129], v[8:9]
	v_lshl_add_u64 v[4:5], s[20:21], 0, v[4:5]
	v_lshl_add_u64 v[4:5], v[4:5], 0, v[162:163]
	v_mov_b32_e32 v2, v247
	v_pk_mul_f32 v[6:7], v[6:7], v[2:3] op_sel_hi:[1,0]
	v_pk_mul_f32 v[8:9], v[8:9], v[2:3] op_sel_hi:[1,0]
	v_cvt_pk_bf16_f32 v6, v6, v7
	v_cvt_pk_bf16_f32 v7, v8, v9
	global_store_dwordx2 v[4:5], v[6:7], off
	v_rcp_f32_e32 v3, v11
	s_nop 0
	v_mul_f32_e32 v7, v115, v3
	v_mul_f32_e32 v6, 0xbfb8aa3b, v116
	v_exp_f32_e32 v8, v6
	v_mul_f32_e32 v6, 0xbfb8aa3b, v117
	v_exp_f32_e32 v9, v6
	v_rcp_f32_e32 v3, v10
	s_nop 0
	v_mul_f32_e32 v6, v114, v3
	v_pk_mul_f32 v[6:7], v[118:119], v[6:7]
	v_pk_add_f32 v[8:9], v[8:9], 1.0 op_sel_hi:[1,0]
	s_nop 0
	v_pk_mul_f32 v[6:7], v[6:7], v[2:3] op_sel_hi:[1,0]
	s_nop 0
	v_cvt_pk_bf16_f32 v6, v6, v7
	v_rcp_f32_e32 v3, v9
	s_nop 0
	v_mul_f32_e32 v9, v117, v3
	v_mul_f32_e32 v7, 0xbfb8aa3b, v106
	v_exp_f32_e32 v10, v7
	v_mul_f32_e32 v7, 0xbfb8aa3b, v107
	v_exp_f32_e32 v11, v7
	v_rcp_f32_e32 v3, v8
	s_nop 0
	v_mul_f32_e32 v8, v116, v3
	v_pk_mul_f32 v[8:9], v[120:121], v[8:9]
	v_pk_add_f32 v[10:11], v[10:11], 1.0 op_sel_hi:[1,0]
	s_nop 0
	v_pk_mul_f32 v[8:9], v[8:9], v[2:3] op_sel_hi:[1,0]
	s_nop 0
	v_cvt_pk_bf16_f32 v7, v8, v9
	global_store_dwordx2 v[4:5], v[6:7], off offset:32
	v_rcp_f32_e32 v3, v11
	s_nop 0
	v_mul_f32_e32 v7, v107, v3
	v_mul_f32_e32 v6, 0xbfb8aa3b, v108
	v_exp_f32_e32 v8, v6
	v_mul_f32_e32 v6, 0xbfb8aa3b, v109
	v_exp_f32_e32 v9, v6
	v_rcp_f32_e32 v3, v10
	s_nop 0
	v_mul_f32_e32 v6, v106, v3
	v_pk_mul_f32 v[6:7], v[110:111], v[6:7]
	v_pk_add_f32 v[8:9], v[8:9], 1.0 op_sel_hi:[1,0]
	s_nop 0
	v_pk_mul_f32 v[6:7], v[6:7], v[2:3] op_sel_hi:[1,0]
	s_nop 0
	v_cvt_pk_bf16_f32 v6, v6, v7
	v_rcp_f32_e32 v3, v9
	s_nop 0
	v_mul_f32_e32 v9, v109, v3
	v_mul_f32_e32 v7, 0xbfb8aa3b, v102
	v_exp_f32_e32 v10, v7
	v_mul_f32_e32 v7, 0xbfb8aa3b, v103
	v_exp_f32_e32 v11, v7
	v_rcp_f32_e32 v3, v8
	s_nop 0
	v_mul_f32_e32 v8, v108, v3
	v_pk_mul_f32 v[8:9], v[112:113], v[8:9]
	v_pk_add_f32 v[10:11], v[10:11], 1.0 op_sel_hi:[1,0]
	s_nop 0
	v_pk_mul_f32 v[8:9], v[8:9], v[2:3] op_sel_hi:[1,0]
	s_nop 0
	v_cvt_pk_bf16_f32 v7, v8, v9
	global_store_dwordx2 v[4:5], v[6:7], off offset:64
	v_rcp_f32_e32 v3, v11
	s_nop 0
	v_mul_f32_e32 v7, v103, v3
	v_mul_f32_e32 v6, 0xbfb8aa3b, v104
	v_exp_f32_e32 v8, v6
	v_mul_f32_e32 v6, 0xbfb8aa3b, v105
	v_exp_f32_e32 v9, v6
	v_rcp_f32_e32 v3, v10
	s_nop 0
	v_mul_f32_e32 v6, v102, v3
	v_pk_mul_f32 v[6:7], v[98:99], v[6:7]
	v_pk_add_f32 v[8:9], v[8:9], 1.0 op_sel_hi:[1,0]
	s_nop 0
	v_pk_mul_f32 v[6:7], v[6:7], v[2:3] op_sel_hi:[1,0]
	s_nop 0
	v_cvt_pk_bf16_f32 v6, v6, v7
	v_rcp_f32_e32 v3, v9
	s_nop 0
	v_mul_f32_e32 v9, v105, v3
	v_rcp_f32_e32 v3, v8
	s_nop 0
	v_mul_f32_e32 v8, v104, v3
	v_pk_mul_f32 v[8:9], v[100:101], v[8:9]
	s_nop 0
	v_pk_mul_f32 v[2:3], v[8:9], v[2:3] op_sel_hi:[1,0]
	s_nop 0
	v_cvt_pk_bf16_f32 v7, v2, v3
	global_store_dwordx2 v[4:5], v[6:7], off offset:96
	s_branch .LBB0_868
